# proj LDS row stride 144 -> 160 bytes (LDK 72 -> 80 halves) in all three variants: conflict-free ds_read_b128 fragment reads; static LDS 46112 -> 51232
# baseline (speedup 1.0000x reference)
_Z11proj_kernelPKfS0_S0_S0_S0_S0_S0_S0_S0_S0_S0_S0_S0_PfS1_PDF16_S1_S0_S0_S2_:
	s_load_dwordx2 s[16:17], s[0:1], 0x90
	s_load_dwordx4 s[4:7], s[0:1], 0x80
	s_cmpk_gt_u32 s2, 0x5f
	s_mov_b64 s[8:9], -1
	s_cbranch_scc0 .LBB0_16
	s_load_dwordx4 s[8:11], s[0:1], 0x58
	s_lshr_b32 s3, s2, 3
	s_cmpk_gt_u32 s2, 0xbf
	s_mov_b64 s[12:13], -1
	s_cbranch_scc0 .LBB0_3
	v_lshlrev_b32_e32 v54, 2, v0
	v_mov_b32_e32 v55, 0
	s_waitcnt lgkmcnt(0)
	v_lshl_add_u64 v[2:3], s[6:7], 0, v[54:55]
	v_lshl_add_u64 v[4:5], s[16:17], 0, v[54:55]
	v_cmp_gt_u32_e32 vcc, 64, v0
	s_load_dwordx4 s[12:15], s[0:1], 0x38
	s_load_dwordx2 s[22:23], s[0:1], 0x10
	v_cndmask_b32_e32 v2, v4, v2, vcc
	v_cndmask_b32_e32 v3, v5, v3, vcc
	global_load_dword v70, v[2:3], off
	v_lshrrev_b32_e32 v2, 2, v0
	v_and_b32_e32 v56, 15, v0
	v_and_b32_e32 v18, 48, v2
	v_or_b32_e32 v68, v18, v56
	v_bfe_u32 v1, v0, 4, 2
	v_lshlrev_b32_e32 v2, 8, v68
	v_mov_b32_e32 v3, v55
	s_lshl_b32 s20, s2, 1
	v_lshl_add_u64 v[2:3], s[8:9], 0, v[2:3]
	v_lshlrev_b32_e32 v4, 5, v1
	v_mov_b32_e32 v5, v55
	s_and_b32 s20, s20, 6
	s_bfe_u32 s21, s2, 0x10003
	v_lshl_add_u64 v[14:15], v[2:3], 0, v[4:5]
	s_sub_i32 s19, s3, 24
	s_or_b32 s21, s21, s20
	v_lshl_add_u64 v[6:7], v[14:15], 0, 16
	s_mov_b64 s[24:25], 0x80
	s_bfe_u32 s18, s2, 0x10002
	s_lshr_b32 s19, s19, 1
	s_lshl_b32 s20, s21, 6
	v_lshl_add_u64 v[10:11], v[14:15], 0, s[24:25]
	s_mov_b64 s[24:25], 0x90
	v_lshlrev_b32_e32 v22, 2, v18
	v_mov_b32_e32 v23, v55
	s_lshl_b32 s21, s21, 8
	v_lshl_add_u64 v[14:15], v[14:15], 0, s[24:25]
	v_lshl_add_u64 v[24:25], s[10:11], 0, v[22:23]
	v_lshlrev_b32_e32 v18, 4, v1
	v_mov_b32_e32 v19, v55
	s_waitcnt lgkmcnt(0)
	s_add_u32 s14, s14, s21
	v_lshl_add_u64 v[18:19], v[24:25], 0, v[18:19]
	s_addc_u32 s15, s15, 0
	v_lshlrev_b32_e32 v26, 2, v56
	v_mov_b32_e32 v27, v55
	v_lshl_add_u64 v[22:23], s[14:15], 0, v[22:23]
	s_mul_i32 s26, s18, 0x180
	v_lshrrev_b32_e32 v57, 4, v0
	v_lshl_add_u64 v[24:25], v[24:25], 0, v[26:27]
	v_lshl_add_u64 v[22:23], v[22:23], 0, v[26:27]
	s_mulk_i32 s19, 0x60
	global_load_dword v69, v[22:23], off
	v_or_b32_e32 v22, s26, v57
	v_add_u32_e32 v22, s19, v22
	v_mov_b32_e32 v23, v55
	v_lshlrev_b64 v[22:23], 11, v[22:23]
	v_and_b32_e32 v72, 60, v54
	v_lshl_add_u64 v[22:23], s[22:23], 0, v[22:23]
	v_lshlrev_b32_e32 v54, 2, v72
	v_lshl_add_u64 v[66:67], v[22:23], 0, v[54:55]
	global_load_dwordx4 v[22:25], v[66:67], off
	s_mov_b32 s14, 0x10000
	v_add_co_u32_e32 v64, vcc, s14, v66
	s_mov_b32 s15, 0x20000
	s_nop 0
	v_addc_co_u32_e32 v65, vcc, 0, v67, vcc
	global_load_dwordx4 v[30:33], v[64:65], off
	v_add_co_u32_e32 v62, vcc, s15, v66
	v_or_b32_e32 v26, s20, v57
	s_nop 0
	v_addc_co_u32_e32 v63, vcc, 0, v67, vcc
	global_load_dwordx4 v[34:37], v[62:63], off
	v_lshlrev_b32_e32 v26, 9, v26
	v_lshl_add_u64 v[26:27], v[26:27], 2, s[12:13]
	v_lshl_add_u64 v[60:61], v[26:27], 0, v[54:55]
	v_add_co_u32_e32 v58, vcc, s14, v60
	global_load_dwordx4 v[38:41], v[60:61], off
	s_nop 0
	v_addc_co_u32_e32 v59, vcc, 0, v61, vcc
	global_load_dwordx4 v[42:45], v[58:59], off
	global_load_dwordx4 v[46:49], v[66:67], off offset:256
	global_load_dwordx4 v[50:53], v[64:65], off offset:256
	global_load_dwordx4 v[74:77], v[62:63], off offset:256
	global_load_dwordx4 v[78:81], v[60:61], off offset:256
	global_load_dwordx4 v[82:85], v[58:59], off offset:256
	global_load_dwordx4 v[86:89], v[66:67], off offset:512
	global_load_dwordx4 v[90:93], v[64:65], off offset:512
	v_lshrrev_b32_e32 v26, 8, v0
	v_mul_u32_u24_e32 v54, 48, v26
	global_load_dwordx4 v[26:29], v[62:63], off offset:512
	global_load_dwordx4 v[94:97], v[60:61], off offset:512
	v_or_b32_e32 v102, v54, v56
	v_and_b32_e32 v56, 48, v0
	s_movk_i32 s14, 0xa0
	v_mad_u32_u24 v73, v68, s14, v56
	v_lshl_or_b32 v1, v1, 2, v54
	v_mul_lo_u32 v1, v1, s14
	v_lshl_add_u32 v1, v68, 1, v1
	s_movk_i32 s15, 0x180
	s_waitcnt vmcnt(13)
	v_cvt_f16_f32_e32 v22, v22
	v_cvt_f16_f32_e32 v25, v25
	v_cvt_pk_f16_f32 v23, v23, v24
	v_mul_u32_u24_e32 v24, 0xa0, v57
	v_pack_b32_f16 v22, v22, v23
	v_alignbit_b32 v23, v25, v23, 16
	v_lshl_add_u32 v72, v72, 1, v24
	s_waitcnt vmcnt(12)
	v_cvt_f16_f32_e32 v25, v30
	v_cvt_f16_f32_e32 v30, v33
	v_cvt_pk_f16_f32 v31, v31, v32
	v_mad_u64_u32 v[56:57], s[12:13], v102, s14, v[56:57]
	v_pack_b32_f16 v24, v25, v31
	v_alignbit_b32 v25, v30, v31, 16
	s_waitcnt vmcnt(11)
	v_cvt_f16_f32_e32 v30, v34
	ds_write2st64_b64 v72, v[22:23], v[24:25] offset1:10
	s_waitcnt vmcnt(8)
	v_cvt_f16_f32_e32 v34, v46
	v_cvt_pk_f16_f32 v23, v35, v36
	v_cvt_f16_f32_e32 v35, v49
	v_cvt_pk_f16_f32 v36, v47, v48
	v_pack_b32_f16 v102, v34, v36
	s_waitcnt vmcnt(7)
	v_cvt_f16_f32_e32 v34, v50
	v_alignbit_b32 v103, v35, v36, 16
	v_cvt_f16_f32_e32 v35, v53
	v_cvt_pk_f16_f32 v36, v51, v52
	v_pack_b32_f16 v104, v34, v36
	s_waitcnt vmcnt(6)
	v_cvt_f16_f32_e32 v34, v74
	v_alignbit_b32 v105, v35, v36, 16
	v_cvt_f16_f32_e32 v35, v77
	v_cvt_pk_f16_f32 v36, v75, v76
	v_pack_b32_f16 v106, v34, v36
	s_waitcnt vmcnt(5)
	v_cvt_f16_f32_e32 v34, v78
	v_alignbit_b32 v107, v35, v36, 16
	v_cvt_f16_f32_e32 v35, v81
	v_cvt_pk_f16_f32 v36, v79, v80
	v_pack_b32_f16 v108, v34, v36
	s_waitcnt vmcnt(4)
	v_cvt_f16_f32_e32 v34, v82
	v_cvt_f16_f32_e32 v24, v37
	v_pack_b32_f16 v22, v30, v23
	v_cvt_f16_f32_e32 v25, v38
	v_cvt_f16_f32_e32 v30, v41
	v_alignbit_b32 v109, v35, v36, 16
	v_cvt_f16_f32_e32 v35, v85
	v_cvt_pk_f16_f32 v36, v83, v84
	v_cvt_pk_f16_f32 v31, v39, v40
	v_pack_b32_f16 v110, v34, v36
	s_waitcnt vmcnt(3)
	v_cvt_f16_f32_e32 v34, v86
	v_alignbit_b32 v23, v24, v23, 16
	v_pack_b32_f16 v24, v25, v31
	v_alignbit_b32 v25, v30, v31, 16
	v_cvt_f16_f32_e32 v30, v42
	v_cvt_f16_f32_e32 v31, v45
	v_alignbit_b32 v111, v35, v36, 16
	v_cvt_pk_f16_f32 v36, v87, v88
	v_cvt_pk_f16_f32 v32, v43, v44
	v_cvt_f16_f32_e32 v35, v89
	v_pack_b32_f16 v114, v34, v36
	s_waitcnt vmcnt(2)
	v_cvt_f16_f32_e32 v34, v90
	v_pack_b32_f16 v30, v30, v32
	v_alignbit_b32 v31, v31, v32, 16
	ds_write2st64_b64 v72, v[22:23], v[24:25] offset0:20 offset1:60
	global_load_dwordx4 v[22:25], v[58:59], off offset:512
	ds_write_b64 v72, v[30:31] offset:35840
	s_waitcnt lgkmcnt(0)
	s_barrier
	global_load_dwordx4 v[30:33], v[66:67], off offset:768
	global_load_dwordx4 v[98:101], v[64:65], off offset:768
	v_cvt_pk_f16_f32 v39, v91, v92
	v_alignbit_b32 v115, v35, v36, 16
	v_cvt_f16_f32_e32 v38, v93
	v_pack_b32_f16 v116, v34, v39
	ds_read_b128 v[34:37], v56
	s_waitcnt vmcnt(4)
	v_cvt_f16_f32_e32 v57, v26
	v_alignbit_b32 v117, v38, v39, 16
	ds_read_b128 v[38:41], v56 offset:2560
	ds_read_b128 v[46:49], v73 offset:30720
	ds_read_b128 v[50:53], v56 offset:5120
	ds_read_b128 v[74:77], v56 offset:64
	ds_read_b128 v[78:81], v73 offset:30784
	v_cvt_f16_f32_e32 v87, v29
	s_waitcnt lgkmcnt(3)
	v_mfma_f32_16x16x32_f16 v[34:37], v[34:37], v[46:49], 0
	v_cvt_pk_f16_f32 v86, v27, v28
	global_load_dwordx4 v[42:45], v[62:63], off offset:768
	ds_read_b128 v[26:29], v56 offset:2624
	v_mfma_f32_16x16x32_f16 v[82:85], v[38:41], v[46:49], 0
	v_pack_b32_f16 v118, v57, v86
	v_alignbit_b32 v119, v87, v86, 16
	ds_read_b128 v[86:89], v56 offset:5184
	s_waitcnt lgkmcnt(4)
	v_mfma_f32_16x16x32_f16 v[50:53], v[50:53], v[46:49], 0
	global_load_dwordx4 v[46:49], v[60:61], off offset:768
	ds_write2st64_b64 v72, v[102:103], v[104:105] offset0:30 offset1:40
	ds_write2st64_b64 v72, v[106:107], v[108:109] offset0:50 offset1:80
	ds_write_b64 v72, v[110:111] offset:46080
	s_waitcnt lgkmcnt(5)
	v_mfma_f32_16x16x32_f16 v[74:77], v[74:77], v[78:81], v[34:37]
	s_waitcnt vmcnt(5)
	v_cvt_f16_f32_e32 v57, v94
	v_cvt_f16_f32_e32 v90, v97
	v_cvt_pk_f16_f32 v91, v95, v96
	global_load_dwordx4 v[34:37], v[58:59], off offset:768
	s_waitcnt lgkmcnt(0)
	s_barrier
	global_load_dwordx4 v[38:41], v[66:67], off offset:1024
	v_pack_b32_f16 v120, v57, v91
	v_alignbit_b32 v121, v90, v91, 16
	global_load_dwordx4 v[90:93], v[64:65], off offset:1024
	v_mfma_f32_16x16x32_f16 v[50:53], v[86:89], v[78:81], v[50:53]
	global_load_dwordx4 v[86:89], v[62:63], off offset:1024
	s_load_dwordx2 s[12:13], s[0:1], 0x78
	s_waitcnt vmcnt(8)
	v_cvt_f16_f32_e32 v22, v22
	v_mfma_f32_16x16x32_f16 v[82:85], v[26:29], v[78:81], v[82:85]
	v_cvt_f16_f32_e32 v25, v25
	v_cvt_pk_f16_f32 v23, v23, v24
	v_pack_b32_f16 v122, v22, v23
	s_waitcnt vmcnt(7)
	v_cvt_f16_f32_e32 v26, v30
	v_cvt_pk_f16_f32 v57, v31, v32
	v_alignbit_b32 v123, v25, v23, 16
	ds_read_b128 v[22:25], v56 offset:15360
	ds_read_b128 v[78:81], v73 offset:40960
	v_cvt_f16_f32_e32 v125, v33
	s_waitcnt vmcnt(6)
	v_cvt_f16_f32_e32 v126, v98
	v_cvt_pk_f16_f32 v127, v99, v100
	v_cvt_f16_f32_e32 v128, v101
	ds_read_b128 v[94:97], v56 offset:15424
	ds_read_b128 v[98:101], v73 offset:41024
	ds_read_b128 v[30:33], v56 offset:17920
	ds_read_b128 v[102:105], v56 offset:17984
	ds_read_b128 v[106:109], v56 offset:20480
	ds_read_b128 v[110:113], v56 offset:20544
	ds_write2st64_b64 v72, v[114:115], v[116:117] offset1:10
	global_load_dwordx4 v[114:117], v[60:61], off offset:1024
	v_pack_b32_f16 v124, v26, v57
	global_load_dwordx4 v[26:29], v[58:59], off offset:1024
	s_waitcnt lgkmcnt(0)
	v_mfma_f32_16x16x32_f16 v[74:77], v[22:25], v[78:81], v[74:77]
	ds_write2st64_b64 v72, v[118:119], v[120:121] offset0:20 offset1:60
	s_waitcnt vmcnt(7)
	v_cvt_f16_f32_e32 v42, v42
	v_cvt_f16_f32_e32 v45, v45
	v_mfma_f32_16x16x32_f16 v[82:85], v[30:33], v[78:81], v[82:85]
	ds_write_b64 v72, v[122:123] offset:35840
	s_waitcnt lgkmcnt(0)
	s_barrier
	global_load_dwordx4 v[22:25], v[66:67], off offset:1280
	global_load_dwordx4 v[30:33], v[64:65], off offset:1280
	v_cvt_pk_f16_f32 v43, v43, v44
	v_alignbit_b32 v125, v125, v57, 16
	v_mfma_f32_16x16x32_f16 v[50:53], v[106:109], v[78:81], v[50:53]
	v_pack_b32_f16 v108, v42, v43
	v_alignbit_b32 v109, v45, v43, 16
	s_waitcnt vmcnt(7)
	v_cvt_f16_f32_e32 v34, v34
	v_cvt_pk_f16_f32 v35, v35, v36
	v_cvt_f16_f32_e32 v36, v37
	v_mfma_f32_16x16x32_f16 v[42:45], v[94:97], v[98:101], v[74:77]
	v_cvt_f16_f32_e32 v57, v46
	s_waitcnt vmcnt(6)
	v_cvt_f16_f32_e32 v37, v41
	v_pack_b32_f16 v106, v126, v127
	v_cvt_f16_f32_e32 v74, v49
	v_cvt_pk_f16_f32 v75, v47, v48
	v_mfma_f32_16x16x32_f16 v[46:49], v[102:105], v[98:101], v[82:85]
	v_pack_b32_f16 v104, v34, v35
	v_cvt_f16_f32_e32 v34, v38
	v_alignbit_b32 v105, v36, v35, 16
	v_cvt_pk_f16_f32 v35, v39, v40
	v_alignbit_b32 v119, v37, v35, 16
	v_pack_b32_f16 v118, v34, v35
	ds_read_b128 v[34:37], v56
	v_pack_b32_f16 v102, v57, v75
	v_alignbit_b32 v103, v74, v75, 16
	ds_read_b128 v[74:77], v56 offset:2560
	ds_read_b128 v[78:81], v73 offset:30720
	s_waitcnt vmcnt(5)
	v_cvt_f16_f32_e32 v38, v90
	v_cvt_f16_f32_e32 v40, v93
	v_mfma_f32_16x16x32_f16 v[50:53], v[110:113], v[98:101], v[50:53]
	v_cvt_pk_f16_f32 v39, v91, v92
	v_pack_b32_f16 v120, v38, v39
	v_alignbit_b32 v121, v40, v39, 16
	ds_read_b128 v[82:85], v56 offset:5120
	ds_read_b128 v[90:93], v56 offset:64
	ds_read_b128 v[94:97], v73 offset:30784
	s_waitcnt lgkmcnt(3)
	v_mfma_f32_16x16x32_f16 v[34:37], v[34:37], v[78:81], v[42:45]
	global_load_dwordx4 v[38:41], v[62:63], off offset:1280
	v_alignbit_b32 v107, v128, v127, 16
	ds_read_b128 v[98:101], v56 offset:2624
	s_waitcnt vmcnt(5)
	v_cvt_f16_f32_e32 v42, v86
	v_cvt_f16_f32_e32 v44, v89
	v_mfma_f32_16x16x32_f16 v[74:77], v[74:77], v[78:81], v[46:49]
	v_cvt_pk_f16_f32 v43, v87, v88
	v_pack_b32_f16 v122, v42, v43
	v_alignbit_b32 v123, v44, v43, 16
	s_waitcnt lgkmcnt(3)
	v_mfma_f32_16x16x32_f16 v[78:81], v[82:85], v[78:81], v[50:53]
	global_load_dwordx4 v[42:45], v[58:59], off offset:1280
	ds_read_b128 v[86:89], v56 offset:5184
	ds_write2st64_b64 v72, v[124:125], v[106:107] offset0:30 offset1:40
	global_load_dwordx4 v[50:53], v[60:61], off offset:1280
	ds_write2st64_b64 v72, v[108:109], v[102:103] offset0:50 offset1:80
	ds_write_b64 v72, v[104:105] offset:46080
	s_waitcnt lgkmcnt(0)
	s_barrier
	global_load_dwordx4 v[46:49], v[66:67], off offset:1536
	global_load_dwordx4 v[82:85], v[64:65], off offset:1536
	v_mfma_f32_16x16x32_f16 v[78:81], v[86:89], v[94:97], v[78:81]
	ds_read_b128 v[86:89], v73 offset:40960
	s_waitcnt vmcnt(8)
	v_cvt_f16_f32_e32 v57, v114
	v_mfma_f32_16x16x32_f16 v[34:37], v[90:93], v[94:97], v[34:37]
	s_waitcnt vmcnt(7)
	v_cvt_f16_f32_e32 v26, v26
	v_cvt_f16_f32_e32 v29, v29
	v_cvt_pk_f16_f32 v27, v27, v28
	v_cvt_f16_f32_e32 v91, v117
	v_pack_b32_f16 v126, v26, v27
	v_alignbit_b32 v127, v29, v27, 16
	ds_read_b128 v[26:29], v56 offset:15360
	v_cvt_pk_f16_f32 v90, v115, v116
	v_pack_b32_f16 v124, v57, v90
	v_mfma_f32_16x16x32_f16 v[74:77], v[98:101], v[94:97], v[74:77]
	v_alignbit_b32 v125, v91, v90, 16
	s_waitcnt vmcnt(5)
	v_cvt_f16_f32_e32 v130, v30
	v_cvt_pk_f16_f32 v131, v31, v32
	v_cvt_f16_f32_e32 v132, v33
	ds_read_b128 v[90:93], v56 offset:15424
	global_load_dwordx4 v[94:97], v[62:63], off offset:1536
	ds_read_b128 v[98:101], v73 offset:41024
	s_waitcnt lgkmcnt(2)
	v_mfma_f32_16x16x32_f16 v[26:29], v[26:29], v[86:89], v[34:37]
	ds_read_b128 v[30:33], v56 offset:17920
	ds_read_b128 v[102:105], v56 offset:17984
	ds_read_b128 v[106:109], v56 offset:20480
	ds_read_b128 v[110:113], v56 offset:20544
	global_load_dwordx4 v[114:117], v[60:61], off offset:1536
	global_load_dwordx4 v[34:37], v[58:59], off offset:1536
	v_cvt_f16_f32_e32 v57, v22
	v_cvt_pk_f16_f32 v128, v23, v24
	v_cvt_f16_f32_e32 v129, v25
	ds_write2st64_b64 v72, v[118:119], v[120:121] offset1:10
	ds_write2st64_b64 v72, v[122:123], v[124:125] offset0:20 offset1:60
	ds_write_b64 v72, v[126:127] offset:35840
	s_waitcnt lgkmcnt(0)
	s_barrier
	global_load_dwordx4 v[22:25], v[66:67], off offset:1792
	v_mfma_f32_16x16x32_f16 v[74:77], v[30:33], v[86:89], v[74:77]
	global_load_dwordx4 v[30:33], v[64:65], off offset:1792
	v_pack_b32_f16 v118, v57, v128
	v_alignbit_b32 v119, v129, v128, 16
	v_mfma_f32_16x16x32_f16 v[64:67], v[106:109], v[86:89], v[78:81]
	v_pack_b32_f16 v120, v130, v131
	v_alignbit_b32 v121, v132, v131, 16
	s_waitcnt vmcnt(9)
	v_cvt_f16_f32_e32 v38, v38
	v_cvt_f16_f32_e32 v41, v41
	v_cvt_pk_f16_f32 v39, v39, v40
	v_mfma_f32_16x16x32_f16 v[78:81], v[90:93], v[98:101], v[26:29]
	v_pack_b32_f16 v106, v38, v39
	v_alignbit_b32 v107, v41, v39, 16
	s_waitcnt vmcnt(8)
	v_cvt_f16_f32_e32 v38, v42
	v_cvt_f16_f32_e32 v40, v45
	v_cvt_pk_f16_f32 v39, v43, v44
	s_waitcnt vmcnt(7)
	v_cvt_f16_f32_e32 v26, v50
	v_cvt_f16_f32_e32 v27, v53
	v_cvt_pk_f16_f32 v28, v51, v52
	v_mfma_f32_16x16x32_f16 v[50:53], v[102:105], v[98:101], v[74:77]
	v_pack_b32_f16 v102, v26, v28
	v_alignbit_b32 v103, v27, v28, 16
	global_load_dwordx4 v[26:29], v[62:63], off offset:1792
	v_pack_b32_f16 v104, v38, v39
	s_waitcnt vmcnt(7)
	v_cvt_f16_f32_e32 v38, v46
	v_alignbit_b32 v105, v40, v39, 16
	v_cvt_f16_f32_e32 v39, v49
	s_waitcnt vmcnt(6)
	v_cvt_f16_f32_e32 v44, v82
	v_cvt_pk_f16_f32 v40, v47, v48
	v_cvt_pk_f16_f32 v48, v83, v84
	v_pack_b32_f16 v38, v38, v40
	v_alignbit_b32 v39, v39, v40, 16
	ds_read_b128 v[40:43], v56
	v_pack_b32_f16 v108, v44, v48
	v_cvt_f16_f32_e32 v49, v85
	ds_read_b128 v[44:47], v56 offset:2560
	ds_read_b128 v[74:77], v73 offset:30720
	ds_read_b128 v[82:85], v56 offset:5120
	global_load_dwordx4 v[60:63], v[60:61], off offset:1792
	v_mfma_f32_16x16x32_f16 v[64:67], v[110:113], v[98:101], v[64:67]
	ds_read_b128 v[86:89], v56 offset:64
	ds_read_b128 v[90:93], v73 offset:30784
	global_load_dwordx4 v[98:101], v[58:59], off offset:1792
	v_alignbit_b32 v109, v49, v48, 16
	s_waitcnt lgkmcnt(3)
	v_mfma_f32_16x16x32_f16 v[40:43], v[40:43], v[74:77], v[78:81]
	s_waitcnt vmcnt(7)
	v_cvt_pk_f16_f32 v57, v95, v96
	s_nop 0
	ds_read_b128 v[78:81], v56 offset:2624
	v_mfma_f32_16x16x32_f16 v[44:47], v[44:47], v[74:77], v[50:53]
	s_waitcnt vmcnt(6)
	v_cvt_f16_f32_e32 v59, v117
	s_waitcnt vmcnt(5)
	v_cvt_f16_f32_e32 v34, v34
	ds_read_b128 v[48:51], v56 offset:5184
	v_cvt_f16_f32_e32 v52, v94
	v_cvt_f16_f32_e32 v53, v97
	v_cvt_f16_f32_e32 v37, v37
	v_cvt_pk_f16_f32 v35, v35, v36
	s_waitcnt lgkmcnt(4)
	v_mfma_f32_16x16x32_f16 v[64:67], v[82:85], v[74:77], v[64:67]
	v_pack_b32_f16 v52, v52, v57
	v_alignbit_b32 v53, v53, v57, 16
	v_cvt_f16_f32_e32 v57, v114
	s_waitcnt lgkmcnt(2)
	v_mfma_f32_16x16x32_f16 v[40:43], v[86:89], v[90:93], v[40:43]
	ds_write2st64_b64 v72, v[118:119], v[120:121] offset0:30 offset1:40
	ds_write2st64_b64 v72, v[106:107], v[102:103] offset0:50 offset1:80
	ds_write_b64 v72, v[104:105] offset:46080
	v_pack_b32_f16 v86, v34, v35
	v_alignbit_b32 v87, v37, v35, 16
	s_waitcnt lgkmcnt(0)
	s_barrier
	ds_read_b128 v[34:37], v56 offset:15360
	v_cvt_pk_f16_f32 v74, v115, v116
	v_pack_b32_f16 v58, v57, v74
	v_alignbit_b32 v59, v59, v74, 16
	v_mfma_f32_16x16x32_f16 v[48:51], v[48:51], v[90:93], v[64:67]
	s_nop 2
	ds_read_b128 v[64:67], v56 offset:17920
	ds_read_b128 v[74:77], v73 offset:40960
	s_waitcnt vmcnt(4)
	v_cvt_f16_f32_e32 v57, v22
	v_cvt_pk_f16_f32 v89, v23, v24
	v_mfma_f32_16x16x32_f16 v[44:47], v[78:81], v[90:93], v[44:47]
	v_cvt_f16_f32_e32 v90, v25
	ds_read_b128 v[22:25], v56 offset:20480
	ds_read_b128 v[78:81], v56 offset:15424
	ds_read_b128 v[82:85], v73 offset:41024
	s_waitcnt vmcnt(3)
	v_cvt_f16_f32_e32 v30, v30
	s_waitcnt lgkmcnt(3)
	v_mfma_f32_16x16x32_f16 v[34:37], v[34:37], v[74:77], v[40:43]
	v_cvt_f16_f32_e32 v33, v33
	v_cvt_pk_f16_f32 v31, v31, v32
	v_pack_b32_f16 v88, v57, v89
	ds_read_b128 v[40:43], v56 offset:17984
	v_mfma_f32_16x16x32_f16 v[44:47], v[64:67], v[74:77], v[44:47]
	ds_read_b128 v[64:67], v56 offset:20544
	v_alignbit_b32 v89, v90, v89, 16
	v_pack_b32_f16 v90, v30, v31
	s_waitcnt lgkmcnt(4)
	v_mfma_f32_16x16x32_f16 v[22:25], v[22:25], v[74:77], v[48:51]
	v_alignbit_b32 v91, v33, v31, 16
	ds_write2st64_b64 v72, v[38:39], v[108:109] offset1:10
	ds_write2st64_b64 v72, v[52:53], v[58:59] offset0:20 offset1:60
	ds_write_b64 v72, v[86:87] offset:35840
	s_waitcnt lgkmcnt(0)
	v_mfma_f32_16x16x32_f16 v[30:33], v[78:81], v[82:85], v[34:37]
	s_barrier
	s_waitcnt vmcnt(2)
	v_cvt_f16_f32_e32 v57, v26
	ds_read_b128 v[34:37], v56
	v_mfma_f32_16x16x32_f16 v[38:41], v[40:43], v[82:85], v[44:47]
	s_nop 2
	ds_read_b128 v[42:45], v56 offset:2560
	ds_read_b128 v[46:49], v73 offset:30720
	v_cvt_pk_f16_f32 v58, v27, v28
	v_cvt_f16_f32_e32 v59, v29
	v_mfma_f32_16x16x32_f16 v[22:25], v[64:67], v[82:85], v[22:25]
	ds_read_b128 v[50:53], v56 offset:5120
	ds_read_b128 v[64:67], v56 offset:64
	ds_read_b128 v[74:77], v73 offset:30784
	ds_read_b128 v[26:29], v56 offset:2624
	s_waitcnt lgkmcnt(4)
	v_mfma_f32_16x16x32_f16 v[30:33], v[34:37], v[46:49], v[30:33]
	v_mfma_f32_16x16x32_f16 v[34:37], v[42:45], v[46:49], v[38:41]
	s_waitcnt vmcnt(1)
	v_cvt_f16_f32_e32 v44, v60
	v_cvt_f16_f32_e32 v45, v63
	v_pack_b32_f16 v42, v57, v58
	s_waitcnt lgkmcnt(3)
	v_mfma_f32_16x16x32_f16 v[22:25], v[50:53], v[46:49], v[22:25]
	v_cvt_pk_f16_f32 v46, v61, v62
	ds_read_b128 v[38:41], v56 offset:5184
	v_pack_b32_f16 v44, v44, v46
	v_alignbit_b32 v45, v45, v46, 16
	s_waitcnt vmcnt(0)
	v_cvt_f16_f32_e32 v46, v98
	s_waitcnt lgkmcnt(1)
	v_mfma_f32_16x16x32_f16 v[26:29], v[26:29], v[74:77], v[34:37]
	v_alignbit_b32 v43, v59, v58, 16
	ds_write2st64_b64 v72, v[88:89], v[90:91] offset0:30 offset1:40
	ds_write2st64_b64 v72, v[42:43], v[44:45] offset0:50 offset1:80
	v_cvt_f16_f32_e32 v35, v101
	v_cvt_pk_f16_f32 v36, v99, v100
	v_pack_b32_f16 v34, v46, v36
	v_mfma_f32_16x16x32_f16 v[30:33], v[64:67], v[74:77], v[30:33]
	v_alignbit_b32 v35, v35, v36, 16
	ds_write_b64 v72, v[34:35] offset:46080
	s_waitcnt lgkmcnt(0)
	s_barrier
	ds_read_b128 v[34:37], v56 offset:15360
	v_mfma_f32_16x16x32_f16 v[22:25], v[38:41], v[74:77], v[22:25]
	ds_read_b128 v[38:41], v73 offset:40960
	ds_read_b128 v[42:45], v56 offset:15424
	ds_read_b128 v[46:49], v73 offset:41024
	s_waitcnt lgkmcnt(2)
	v_mfma_f32_16x16x32_f16 v[30:33], v[34:37], v[38:41], v[30:33]
	ds_read_b128 v[34:37], v56 offset:17920
	ds_read_b128 v[50:53], v56 offset:17984
	s_waitcnt lgkmcnt(2)
	v_mfma_f32_16x16x32_f16 v[30:33], v[42:45], v[46:49], v[30:33]
	s_waitcnt lgkmcnt(1)
	v_mfma_f32_16x16x32_f16 v[26:29], v[34:37], v[38:41], v[26:29]
	ds_read_b128 v[34:37], v56 offset:20480
	ds_read_b128 v[56:59], v56 offset:20544
	s_waitcnt vmcnt(0)
	s_waitcnt lgkmcnt(0)
	s_nop 2
	v_add_f32_e32 v2, v30, v69
	v_mfma_f32_16x16x32_f16 v[26:29], v[50:53], v[46:49], v[26:29]
	v_cvt_f16_f32_e32 v2, v2
	v_add_f32_e32 v3, v31, v69
	v_cvt_f16_f32_e32 v3, v3
	v_mfma_f32_16x16x32_f16 v[22:25], v[34:37], v[38:41], v[22:25]
	v_add_f32_e32 v4, v32, v69
	v_cvt_f16_f32_e32 v4, v4
	v_add_f32_e32 v5, v33, v69
	v_cvt_f16_f32_e32 v5, v5
	s_barrier
	ds_write_b16 v1, v2
	ds_write_b16 v1, v3 offset:160
	ds_write_b16 v1, v4 offset:320
	ds_write_b16 v1, v5 offset:480
	v_add_f32_e32 v2, v26, v69
	v_mfma_f32_16x16x32_f16 v[22:25], v[56:59], v[46:49], v[22:25]
	v_cvt_f16_f32_e32 v2, v2
	v_add_f32_e32 v3, v27, v69
	v_cvt_f16_f32_e32 v3, v3
	v_add_f32_e32 v4, v28, v69
	v_cvt_f16_f32_e32 v4, v4
	v_add_f32_e32 v5, v29, v69
	v_cvt_f16_f32_e32 v5, v5
	ds_write_b16 v1, v2 offset:2560
	ds_write_b16 v1, v3 offset:2720
	ds_write_b16 v1, v4 offset:2880
	ds_write_b16 v1, v5 offset:3040
	v_add_f32_e32 v2, v22, v69
	v_cvt_f16_f32_e32 v2, v2
	v_add_f32_e32 v3, v23, v69
	v_cvt_f16_f32_e32 v3, v3
	v_add_f32_e32 v4, v24, v69
	v_cvt_f16_f32_e32 v4, v4
	v_add_f32_e32 v5, v25, v69
	v_cvt_f16_f32_e32 v5, v5
	ds_write_b16 v1, v2 offset:5120
	ds_write_b16 v1, v3 offset:5280
	ds_write_b16 v1, v4 offset:5440
	ds_write_b16 v1, v5 offset:5600
	v_and_b32_e32 v2, 7, v0
	v_mul_u32_u24_e32 v10, 12, v2
	v_mul_u32_u24_e32 v2, 0x3c0, v2
	v_lshrrev_b32_e32 v1, 3, v0
	v_lshlrev_b32_e32 v2, 1, v2
	v_lshl_add_u32 v3, v1, 1, v2
	s_waitcnt lgkmcnt(0)
	s_barrier
	ds_read_u16 v2, v3
	ds_read_u16 v4, v3 offset:160
	ds_read_u16 v5, v3 offset:320
	ds_read_u16 v6, v3 offset:480
	ds_read_u16 v7, v3 offset:640
	ds_read_u16 v8, v3 offset:800
	ds_read_u16 v9, v3 offset:960
	ds_read_u16 v11, v3 offset:1120
	ds_read_u16 v12, v3 offset:1280
	ds_read_u16 v13, v3 offset:1440
	ds_read_u16 v14, v3 offset:1600
	ds_read_u16 v15, v3 offset:1760
	v_lshl_or_b32 v1, s18, 9, v1
	s_waitcnt lgkmcnt(10)
	v_lshl_or_b32 v2, v4, 16, v2
	s_waitcnt lgkmcnt(6)
	v_lshl_or_b32 v4, v8, 16, v7
	v_or_b32_e32 v1, s20, v1
	v_mov_b32_e32 v8, s19
	v_mad_u32_u24 v54, v1, s15, v8
	v_lshl_or_b32 v3, v6, 16, v5
	s_waitcnt lgkmcnt(4)
	v_lshl_or_b32 v5, v11, 16, v9
	v_lshl_add_u64 v[8:9], v[54:55], 1, s[12:13]
	v_lshlrev_b32_e32 v54, 1, v10
	v_lshl_add_u64 v[8:9], v[8:9], 0, v[54:55]
	s_waitcnt lgkmcnt(2)
	v_lshl_or_b32 v6, v13, 16, v12
	s_waitcnt lgkmcnt(0)
	v_lshl_or_b32 v7, v15, 16, v14
	global_store_dwordx4 v[8:9], v[2:5], off
	global_store_dwordx2 v[8:9], v[6:7], off offset:16
	s_mov_b64 s[12:13], 0
.LBB0_3:
	s_andn2_b64 vcc, exec, s[12:13]
	s_cbranch_vccnz .LBB0_15
	v_lshlrev_b32_e32 v56, 2, v0
	v_mov_b32_e32 v57, 0
	s_waitcnt lgkmcnt(0)
	v_lshl_add_u64 v[2:3], s[6:7], 0, v[56:57]
	v_lshl_add_u64 v[4:5], s[16:17], 0, v[56:57]
	v_cmp_gt_u32_e32 vcc, 64, v0
	s_load_dwordx4 s[12:15], s[0:1], 0x28
	s_load_dwordx2 s[22:23], s[0:1], 0x8
	v_cndmask_b32_e32 v2, v4, v2, vcc
	v_cndmask_b32_e32 v3, v5, v3, vcc
	global_load_dword v54, v[2:3], off
	v_lshrrev_b32_e32 v2, 2, v0
	v_and_b32_e32 v70, 15, v0
	v_and_b32_e32 v55, 48, v2
	v_or_b32_e32 v66, v55, v70
	v_bfe_u32 v1, v0, 4, 2
	v_lshlrev_b32_e32 v2, 8, v66
	v_mov_b32_e32 v3, v57
	v_lshl_add_u64 v[2:3], s[8:9], 0, v[2:3]
	v_lshlrev_b32_e32 v4, 5, v1
	v_mov_b32_e32 v5, v57
	s_add_i32 s3, s3, -12
	s_lshl_b32 s18, s2, 1
	v_lshl_add_u64 v[2:3], v[2:3], 0, v[4:5]
	s_bfe_u32 s20, s2, 0x10002
	s_ashr_i32 s3, s3, 1
	s_and_b32 s18, s18, 6
	s_bfe_u32 s19, s2, 0x10003
	global_load_dwordx4 v[14:17], v[2:3], off
	v_lshl_add_u64 v[4:5], v[2:3], 0, 16
	s_mov_b64 s[8:9], 0x80
	s_or_b32 s19, s19, s18
	s_lshl_b32 s18, s3, 6
	s_mul_i32 s21, s20, 0x180
	global_load_dwordx4 v[18:21], v[4:5], off
	v_lshl_add_u64 v[4:5], v[2:3], 0, s[8:9]
	s_mov_b64 s[8:9], 0x90
	s_add_i32 s21, s18, s21
	s_lshl_b32 s20, s20, 3
	v_lshl_add_u64 v[2:3], v[2:3], 0, s[8:9]
	v_lshlrev_b32_e32 v22, 2, v55
	v_mov_b32_e32 v23, v57
	s_lshl_b32 s8, s19, 8
	global_load_dwordx4 v[6:9], v[4:5], off
	v_lshl_add_u64 v[24:25], s[10:11], 0, v[22:23]
	v_and_b32_e32 v72, 48, v0
	v_mov_b32_e32 v73, v57
	s_waitcnt lgkmcnt(0)
	s_add_u32 s8, s14, s8
	global_load_dwordx4 v[10:13], v[2:3], off
	v_lshl_add_u64 v[2:3], v[24:25], 0, v[72:73]
	s_addc_u32 s9, s15, 0
	global_load_dwordx4 v[2:5], v[2:3], off
	v_lshlrev_b32_e32 v26, 2, v70
	v_mov_b32_e32 v27, v57
	v_lshl_add_u64 v[22:23], s[8:9], 0, v[22:23]
	v_lshl_add_u64 v[24:25], v[24:25], 0, v[26:27]
	global_load_dword v68, v[24:25], off
	v_lshl_add_u64 v[22:23], v[22:23], 0, v[26:27]
	v_lshrrev_b32_e32 v71, 4, v0
	global_load_dword v67, v[22:23], off
	v_or_b32_e32 v22, s21, v71
	v_ashrrev_i32_e32 v23, 31, v22
	v_lshlrev_b64 v[22:23], 11, v[22:23]
	v_and_b32_e32 v73, 60, v56
	v_lshl_add_u64 v[22:23], s[22:23], 0, v[22:23]
	v_lshlrev_b32_e32 v56, 2, v73
	v_lshl_add_u64 v[62:63], v[22:23], 0, v[56:57]
	global_load_dwordx4 v[22:25], v[62:63], off
	s_mov_b32 s8, 0x10000
	v_add_co_u32_e32 v64, vcc, s8, v62
	v_lshlrev_b32_e32 v30, 9, v71
	s_nop 0
	v_addc_co_u32_e32 v65, vcc, 0, v63, vcc
	global_load_dwordx4 v[26:29], v[64:65], off
	v_lshl_or_b32 v30, s19, 15, v30
	v_mov_b32_e32 v31, v57
	v_lshl_add_u64 v[30:31], v[30:31], 2, s[12:13]
	v_lshl_add_u64 v[60:61], v[30:31], 0, v[56:57]
	global_load_dwordx4 v[30:33], v[60:61], off
	v_add_co_u32_e32 v58, vcc, s8, v60
	v_lshrrev_b32_e32 v56, 3, v0
	s_nop 0
	v_addc_co_u32_e32 v59, vcc, 0, v61, vcc
	global_load_dwordx4 v[34:37], v[58:59], off
	global_load_dwordx4 v[38:41], v[62:63], off offset:256
	global_load_dwordx4 v[42:45], v[64:65], off offset:256
	global_load_dwordx4 v[46:49], v[60:61], off offset:256
	global_load_dwordx4 v[50:53], v[58:59], off offset:256
	v_and_b32_e32 v69, 32, v56
	v_or_b32_e32 v56, v69, v70
	v_mul_u32_u24_e32 v70, 0xa0, v71
	v_lshl_add_u32 v71, v73, 1, v70
	s_movk_i32 s8, 0xa0
	s_or_b32 s12, s19, s20
	s_lshl_b32 s13, s12, 4
	v_cmp_lt_u32_e32 vcc, 63, v0
	s_waitcnt vmcnt(7)
	v_cvt_f16_f32_e32 v22, v22
	v_cvt_f16_f32_e32 v25, v25
	v_cvt_pk_f16_f32 v23, v23, v24
	v_pack_b32_f16 v74, v22, v23
	v_alignbit_b32 v75, v25, v23, 16
	global_load_dwordx4 v[22:25], v[62:63], off offset:512
	s_waitcnt vmcnt(7)
	v_cvt_f16_f32_e32 v26, v26
	v_cvt_f16_f32_e32 v73, v29
	v_cvt_pk_f16_f32 v70, v27, v28
	v_pack_b32_f16 v76, v26, v70
	global_load_dwordx4 v[26:29], v[64:65], off offset:512
	s_waitcnt vmcnt(7)
	v_cvt_f16_f32_e32 v30, v30
	v_alignbit_b32 v77, v73, v70, 16
	v_cvt_f16_f32_e32 v73, v33
	s_waitcnt vmcnt(6)
	v_cvt_f16_f32_e32 v34, v34
	v_cvt_f16_f32_e32 v37, v37
	v_cvt_pk_f16_f32 v70, v31, v32
	ds_write2st64_b64 v71, v[74:75], v[76:77] offset1:10
	v_pack_b32_f16 v74, v30, v70
	global_load_dwordx4 v[30:33], v[60:61], off offset:512
	v_cvt_pk_f16_f32 v35, v35, v36
	v_alignbit_b32 v75, v73, v70, 16
	v_pack_b32_f16 v34, v34, v35
	v_alignbit_b32 v35, v37, v35, 16
	ds_write2st64_b64 v71, v[74:75], v[34:35] offset0:60 offset1:70
	global_load_dwordx4 v[34:37], v[58:59], off offset:512
	v_mad_u32_u24 v70, v56, s8, v72
	s_waitcnt lgkmcnt(0)
	s_barrier
	ds_read_b128 v[74:77], v70
	s_waitcnt vmcnt(7)
	v_cvt_f16_f32_e32 v38, v38
	v_cvt_f16_f32_e32 v41, v41
	v_cvt_pk_f16_f32 v39, v39, v40
	v_mad_u32_u24 v72, v66, s8, v72
	v_pack_b32_f16 v38, v38, v39
	v_alignbit_b32 v39, v41, v39, 16
	s_waitcnt vmcnt(6)
	v_cvt_f16_f32_e32 v40, v42
	v_cvt_f16_f32_e32 v41, v45
	ds_read_b128 v[78:81], v72 offset:30720
	ds_read_b128 v[82:85], v70 offset:64
	ds_read_b128 v[86:89], v72 offset:30784
	v_cvt_pk_f16_f32 v42, v43, v44
	s_waitcnt lgkmcnt(2)
	v_mfma_f32_16x16x32_f16 v[74:77], v[74:77], v[78:81], 0
	ds_read_b128 v[90:93], v70 offset:2560
	ds_read_b128 v[94:97], v70 offset:2624
	v_pack_b32_f16 v40, v40, v42
	v_alignbit_b32 v41, v41, v42, 16
	global_load_dwordx4 v[42:45], v[62:63], off offset:768
	s_waitcnt lgkmcnt(2)
	v_mfma_f32_16x16x32_f16 v[74:77], v[82:85], v[86:89], v[74:77]
	s_waitcnt vmcnt(6)
	v_cvt_f16_f32_e32 v46, v46
	v_cvt_pk_f16_f32 v47, v47, v48
	v_cvt_f16_f32_e32 v48, v49
	s_waitcnt vmcnt(5)
	v_cvt_f16_f32_e32 v73, v50
	v_cvt_f16_f32_e32 v84, v53
	v_cvt_pk_f16_f32 v85, v51, v52
	global_load_dwordx4 v[50:53], v[64:65], off offset:768
	v_pack_b32_f16 v82, v46, v47
	v_alignbit_b32 v83, v48, v47, 16
	global_load_dwordx4 v[46:49], v[60:61], off offset:768
	ds_write2st64_b64 v71, v[38:39], v[40:41] offset0:20 offset1:30
	v_pack_b32_f16 v38, v73, v85
	v_alignbit_b32 v39, v84, v85, 16
	ds_write2st64_b64 v71, v[82:83], v[38:39] offset0:80 offset1:90
	global_load_dwordx4 v[38:41], v[58:59], off offset:768
	s_waitcnt lgkmcnt(0)
	s_barrier
	ds_read_b128 v[82:85], v70 offset:10240
	v_mfma_f32_16x16x32_f16 v[78:81], v[90:93], v[78:81], 0
	s_waitcnt vmcnt(7)
	v_cvt_f16_f32_e32 v22, v22
	v_mfma_f32_16x16x32_f16 v[78:81], v[94:97], v[86:89], v[78:81]
	ds_read_b128 v[86:89], v72 offset:40960
	ds_read_b128 v[90:93], v70 offset:10304
	ds_read_b128 v[94:97], v72 offset:41024
	v_cvt_f16_f32_e32 v25, v25
	v_cvt_pk_f16_f32 v23, v23, v24
	s_waitcnt lgkmcnt(2)
	v_mfma_f32_16x16x32_f16 v[74:77], v[82:85], v[86:89], v[74:77]
	ds_read_b128 v[82:85], v70 offset:12800
	ds_read_b128 v[98:101], v70 offset:12864
	s_waitcnt vmcnt(6)
	v_cvt_f16_f32_e32 v24, v29
	s_waitcnt vmcnt(4)
	v_cvt_f16_f32_e32 v34, v34
	s_waitcnt lgkmcnt(1)
	v_mfma_f32_16x16x32_f16 v[78:81], v[82:85], v[86:89], v[78:81]
	v_pack_b32_f16 v82, v22, v23
	v_cvt_f16_f32_e32 v22, v26
	v_alignbit_b32 v83, v25, v23, 16
	v_cvt_pk_f16_f32 v23, v27, v28
	v_alignbit_b32 v85, v24, v23, 16
	v_pack_b32_f16 v84, v22, v23
	v_cvt_f16_f32_e32 v26, v30
	v_cvt_f16_f32_e32 v27, v33
	global_load_dwordx4 v[22:25], v[62:63], off offset:1024
	v_cvt_pk_f16_f32 v28, v31, v32
	v_cvt_pk_f16_f32 v35, v35, v36
	v_cvt_f16_f32_e32 v36, v37
	v_pack_b32_f16 v86, v26, v28
	v_alignbit_b32 v87, v27, v28, 16
	global_load_dwordx4 v[26:29], v[64:65], off offset:1024
	v_pack_b32_f16 v34, v34, v35
	v_alignbit_b32 v35, v36, v35, 16
	global_load_dwordx4 v[30:33], v[60:61], off offset:1024
	ds_write2st64_b64 v71, v[86:87], v[34:35] offset0:60 offset1:70
	global_load_dwordx4 v[34:37], v[58:59], off offset:1024
	ds_write2st64_b64 v71, v[82:83], v[84:85] offset1:10
	s_waitcnt lgkmcnt(0)
	s_barrier
	ds_read_b128 v[82:85], v70
	v_mfma_f32_16x16x32_f16 v[74:77], v[90:93], v[94:97], v[74:77]
	s_waitcnt vmcnt(7)
	v_cvt_f16_f32_e32 v42, v42
	v_cvt_pk_f16_f32 v43, v43, v44
	v_cvt_f16_f32_e32 v45, v45
	v_mfma_f32_16x16x32_f16 v[78:81], v[98:101], v[94:97], v[78:81]
	ds_read_b128 v[86:89], v72 offset:30720
	ds_read_b128 v[90:93], v70 offset:64
	ds_read_b128 v[94:97], v72 offset:30784
	s_waitcnt vmcnt(6)
	v_cvt_pk_f16_f32 v44, v51, v52
	s_waitcnt vmcnt(5)
	v_cvt_pk_f16_f32 v47, v47, v48
	s_waitcnt lgkmcnt(2)
	v_mfma_f32_16x16x32_f16 v[74:77], v[82:85], v[86:89], v[74:77]
	ds_read_b128 v[82:85], v70 offset:2560
	ds_read_b128 v[98:101], v70 offset:2624
	s_waitcnt vmcnt(4)
	v_cvt_pk_f16_f32 v48, v39, v40
	s_waitcnt vmcnt(3)
	v_cvt_f16_f32_e32 v22, v22
	s_waitcnt lgkmcnt(1)
	v_mfma_f32_16x16x32_f16 v[78:81], v[82:85], v[86:89], v[78:81]
	v_pack_b32_f16 v82, v42, v43
	v_cvt_f16_f32_e32 v42, v50
	v_alignbit_b32 v83, v45, v43, 16
	v_cvt_f16_f32_e32 v43, v53
	v_mfma_f32_16x16x32_f16 v[74:77], v[90:93], v[94:97], v[74:77]
	v_pack_b32_f16 v50, v42, v44
	v_cvt_f16_f32_e32 v42, v46
	v_alignbit_b32 v51, v43, v44, 16
	v_cvt_f16_f32_e32 v46, v49
	ds_write2st64_b64 v71, v[82:83], v[50:51] offset0:20 offset1:30
	v_pack_b32_f16 v52, v42, v47
	global_load_dwordx4 v[42:45], v[62:63], off offset:1280
	v_alignbit_b32 v53, v46, v47, 16
	v_cvt_f16_f32_e32 v46, v38
	v_cvt_f16_f32_e32 v47, v41
	global_load_dwordx4 v[38:41], v[64:65], off offset:1280
	s_waitcnt lgkmcnt(1)
	v_mfma_f32_16x16x32_f16 v[78:81], v[98:101], v[94:97], v[78:81]
	v_pack_b32_f16 v84, v46, v48
	v_alignbit_b32 v85, v47, v48, 16
	global_load_dwordx4 v[46:49], v[60:61], off offset:1280
	ds_write2st64_b64 v71, v[52:53], v[84:85] offset0:80 offset1:90
	global_load_dwordx4 v[50:53], v[58:59], off offset:1280
	s_waitcnt lgkmcnt(0)
	s_barrier
	ds_read_b128 v[82:85], v70 offset:10240
	ds_read_b128 v[86:89], v72 offset:40960
	ds_read_b128 v[90:93], v70 offset:10304
	ds_read_b128 v[94:97], v72 offset:41024
	s_waitcnt lgkmcnt(2)
	v_mfma_f32_16x16x32_f16 v[74:77], v[82:85], v[86:89], v[74:77]
	ds_read_b128 v[82:85], v70 offset:12800
	ds_read_b128 v[98:101], v70 offset:12864
	v_cvt_pk_f16_f32 v73, v23, v24
	s_waitcnt vmcnt(6)
	v_cvt_f16_f32_e32 v26, v26
	s_waitcnt lgkmcnt(1)
	v_mfma_f32_16x16x32_f16 v[78:81], v[82:85], v[86:89], v[78:81]
	v_cvt_f16_f32_e32 v83, v25
	v_pack_b32_f16 v82, v22, v73
	global_load_dwordx4 v[22:25], v[62:63], off offset:1536
	v_cvt_f16_f32_e32 v85, v29
	v_alignbit_b32 v83, v83, v73, 16
	v_cvt_pk_f16_f32 v73, v27, v28
	v_pack_b32_f16 v84, v26, v73
	global_load_dwordx4 v[26:29], v[64:65], off offset:1536
	v_alignbit_b32 v85, v85, v73, 16
	s_waitcnt vmcnt(7)
	v_cvt_f16_f32_e32 v73, v30
	v_cvt_f16_f32_e32 v87, v33
	s_waitcnt vmcnt(6)
	v_cvt_f16_f32_e32 v34, v34
	v_cvt_pk_f16_f32 v88, v31, v32
	v_cvt_pk_f16_f32 v89, v35, v36
	global_load_dwordx4 v[30:33], v[60:61], off offset:1536
	v_pack_b32_f16 v86, v73, v88
	v_alignbit_b32 v87, v87, v88, 16
	v_cvt_f16_f32_e32 v73, v37
	v_pack_b32_f16 v88, v34, v89
	global_load_dwordx4 v[34:37], v[58:59], off offset:1536
	ds_write2st64_b64 v71, v[82:83], v[84:85] offset1:10
	v_alignbit_b32 v89, v73, v89, 16
	ds_write2st64_b64 v71, v[86:87], v[88:89] offset0:60 offset1:70
	s_waitcnt lgkmcnt(0)
	s_barrier
	global_load_dwordx4 v[82:85], v[62:63], off offset:1792
	ds_read_b128 v[86:89], v70
	global_load_dwordx4 v[62:65], v[64:65], off offset:1792
	v_mfma_f32_16x16x32_f16 v[74:77], v[90:93], v[94:97], v[74:77]
	s_waitcnt vmcnt(9)
	v_cvt_pk_f16_f32 v73, v43, v44
	v_mfma_f32_16x16x32_f16 v[78:81], v[98:101], v[94:97], v[78:81]
	ds_read_b128 v[90:93], v72 offset:30720
	ds_read_b128 v[94:97], v70 offset:64
	ds_read_b128 v[98:101], v72 offset:30784
	s_waitcnt vmcnt(8)
	v_cvt_f16_f32_e32 v41, v41
	s_waitcnt lgkmcnt(2)
	v_mfma_f32_16x16x32_f16 v[74:77], v[86:89], v[90:93], v[74:77]
	ds_read_b128 v[86:89], v70 offset:2560
	ds_read_b128 v[102:105], v70 offset:2624
	s_waitcnt vmcnt(7)
	v_cvt_f16_f32_e32 v46, v46
	s_waitcnt lgkmcnt(1)
	v_mfma_f32_16x16x32_f16 v[78:81], v[86:89], v[90:93], v[78:81]
	global_load_dwordx4 v[86:89], v[60:61], off offset:1792
	v_cvt_f16_f32_e32 v60, v42
	v_cvt_f16_f32_e32 v61, v45
	global_load_dwordx4 v[42:45], v[58:59], off offset:1792
	v_cvt_f16_f32_e32 v49, v49
	v_cvt_pk_f16_f32 v47, v47, v48
	v_cvt_f16_f32_e32 v90, v38
	v_pack_b32_f16 v46, v46, v47
	s_waitcnt vmcnt(8)
	v_cvt_f16_f32_e32 v48, v50
	v_alignbit_b32 v47, v49, v47, 16
	v_cvt_f16_f32_e32 v49, v53
	v_pack_b32_f16 v38, v60, v73
	v_cvt_pk_f16_f32 v91, v39, v40
	v_cvt_pk_f16_f32 v50, v51, v52
	v_alignbit_b32 v39, v61, v73, 16
	v_pack_b32_f16 v40, v90, v91
	v_alignbit_b32 v41, v41, v91, 16
	v_pack_b32_f16 v48, v48, v50
	v_alignbit_b32 v49, v49, v50, 16
	ds_write2st64_b64 v71, v[38:39], v[40:41] offset0:20 offset1:30
	s_waitcnt vmcnt(7)
	v_cvt_f16_f32_e32 v22, v22
	v_cvt_f16_f32_e32 v25, v25
	v_cvt_pk_f16_f32 v23, v23, v24
	ds_write2st64_b64 v71, v[46:47], v[48:49] offset0:80 offset1:90
	v_pack_b32_f16 v58, v22, v23
	s_waitcnt vmcnt(6)
	v_cvt_f16_f32_e32 v22, v26
	v_alignbit_b32 v59, v25, v23, 16
	v_cvt_pk_f16_f32 v23, v27, v28
	v_cvt_f16_f32_e32 v24, v29
	v_pack_b32_f16 v60, v22, v23
	s_waitcnt lgkmcnt(0)
	s_barrier
	s_waitcnt vmcnt(5)
	v_cvt_f16_f32_e32 v22, v30
	v_cvt_f16_f32_e32 v25, v33
	v_alignbit_b32 v61, v24, v23, 16
	v_cvt_pk_f16_f32 v23, v31, v32
	v_pack_b32_f16 v90, v22, v23
	s_waitcnt vmcnt(4)
	v_cvt_f16_f32_e32 v26, v34
	v_cvt_f16_f32_e32 v27, v37
	v_cvt_pk_f16_f32 v28, v35, v36
	v_alignbit_b32 v91, v25, v23, 16
	v_mfma_f32_16x16x32_f16 v[22:25], v[102:105], v[98:101], v[78:81]
	s_waitcnt vmcnt(3)
	v_cvt_f16_f32_e32 v30, v82
	s_nop 0
	v_pack_b32_f16 v78, v26, v28
	v_alignbit_b32 v79, v27, v28, 16
	ds_read_b128 v[26:29], v70 offset:10240
	v_cvt_f16_f32_e32 v31, v85
	s_waitcnt vmcnt(2)
	v_cvt_f16_f32_e32 v50, v62
	v_cvt_pk_f16_f32 v32, v83, v84
	v_cvt_pk_f16_f32 v63, v63, v64
	v_mfma_f32_16x16x32_f16 v[74:77], v[94:97], v[98:101], v[74:77]
	v_pack_b32_f16 v80, v30, v32
	v_alignbit_b32 v81, v31, v32, 16
	ds_read_b128 v[30:33], v72 offset:40960
	ds_read_b128 v[34:37], v70 offset:12800
	ds_read_b128 v[38:41], v70 offset:10304
	ds_read_b128 v[46:49], v72 offset:41024
	v_pack_b32_f16 v62, v50, v63
	ds_read_b128 v[50:53], v70 offset:12864
	s_waitcnt lgkmcnt(4)
	v_mfma_f32_16x16x32_f16 v[26:29], v[26:29], v[30:33], v[74:77]
	ds_write2st64_b64 v71, v[58:59], v[60:61] offset1:10
	ds_write2st64_b64 v71, v[90:91], v[78:79] offset0:60 offset1:70
	s_waitcnt lgkmcnt(0)
	s_barrier
	v_mfma_f32_16x16x32_f16 v[22:25], v[34:37], v[30:33], v[22:25]
	ds_read_b128 v[30:33], v70
	v_cvt_f16_f32_e32 v64, v65
	v_mfma_f32_16x16x32_f16 v[26:29], v[38:41], v[46:49], v[26:29]
	ds_read_b128 v[34:37], v70 offset:2560
	ds_read_b128 v[38:41], v72 offset:30720
	v_alignbit_b32 v63, v64, v63, 16
	v_mfma_f32_16x16x32_f16 v[22:25], v[50:53], v[46:49], v[22:25]
	ds_read_b128 v[46:49], v70 offset:64
	ds_read_b128 v[50:53], v72 offset:30784
	s_waitcnt vmcnt(1)
	v_cvt_f16_f32_e32 v58, v86
	v_cvt_f16_f32_e32 v60, v89
	s_waitcnt lgkmcnt(2)
	v_mfma_f32_16x16x32_f16 v[22:25], v[34:37], v[38:41], v[22:25]
	s_waitcnt vmcnt(0)
	v_cvt_f16_f32_e32 v36, v42
	v_cvt_f16_f32_e32 v37, v45
	v_cvt_pk_f16_f32 v59, v87, v88
	v_mfma_f32_16x16x32_f16 v[26:29], v[30:33], v[38:41], v[26:29]
	ds_read_b128 v[30:33], v70 offset:2624
	v_cvt_pk_f16_f32 v38, v43, v44
	v_pack_b32_f16 v34, v58, v59
	v_alignbit_b32 v35, v60, v59, 16
	v_pack_b32_f16 v36, v36, v38
	v_alignbit_b32 v37, v37, v38, 16
	ds_write2st64_b64 v71, v[80:81], v[62:63] offset0:20 offset1:30
	ds_write2st64_b64 v71, v[34:35], v[36:37] offset0:80 offset1:90
	s_waitcnt lgkmcnt(0)
	s_barrier
	ds_read_b128 v[34:37], v70 offset:10240
	v_mfma_f32_16x16x32_f16 v[26:29], v[46:49], v[50:53], v[26:29]
	v_mfma_f32_16x16x32_f16 v[22:25], v[30:33], v[50:53], v[22:25]
	ds_read_b128 v[30:33], v72 offset:40960
	ds_read_b128 v[38:41], v70 offset:10304
	ds_read_b128 v[42:45], v72 offset:41024
	s_waitcnt lgkmcnt(2)
	v_mfma_f32_16x16x32_f16 v[26:29], v[34:37], v[30:33], v[26:29]
	ds_read_b128 v[34:37], v70 offset:12800
	ds_read_b128 v[46:49], v70 offset:12864
	s_waitcnt vmcnt(0)
	s_waitcnt lgkmcnt(0)
	v_mfma_f32_16x16x32_f16 v[22:25], v[34:37], v[30:33], v[22:25]
	v_lshl_or_b32 v30, v1, 2, v69
	v_mul_u32_u24_e32 v30, 0xa0, v30
	v_lshl_add_u32 v30, v66, 1, v30
	v_mfma_f32_16x16x32_f16 v[26:29], v[38:41], v[42:45], v[26:29]
	v_cvt_pk_f16_f32 v21, v20, v21
	v_cvt_pk_f16_f32 v20, v18, v19
	v_cvt_pk_f16_f32 v19, v16, v17
	v_mfma_f32_16x16x32_f16 v[22:25], v[46:49], v[42:45], v[22:25]
	v_cvt_pk_f16_f32 v18, v14, v15
	s_nop 2
	v_add_f32_e32 v26, v26, v67
	v_cvt_f16_f32_e32 v26, v26
	v_add_f32_e32 v27, v27, v67
	v_cvt_f16_f32_e32 v27, v27
	v_add_f32_e32 v22, v22, v67
	v_cvt_f16_f32_e32 v22, v22
	v_add_f32_e32 v23, v23, v67
	v_add_f32_e32 v28, v28, v67
	v_cvt_f16_f32_e32 v23, v23
	v_add_f32_e32 v24, v24, v67
	v_cvt_f16_f32_e32 v28, v28
	v_add_f32_e32 v29, v29, v67
	v_cvt_f16_f32_e32 v24, v24
	v_add_f32_e32 v25, v25, v67
	v_cvt_f16_f32_e32 v29, v29
	v_cvt_f16_f32_e32 v25, v25
	s_barrier
	ds_write_b16 v30, v26
	ds_write_b16 v30, v27 offset:160
	ds_write_b16 v30, v28 offset:320
	ds_write_b16 v30, v29 offset:480
	ds_write_b16 v30, v22 offset:2560
	ds_write_b16 v30, v23 offset:2720
	ds_write_b16 v30, v24 offset:2880
	ds_write_b16 v30, v25 offset:3040
	s_waitcnt lgkmcnt(0)
	s_barrier
	ds_read_b128 v[14:17], v70
	ds_read_b128 v[22:25], v70 offset:64
	v_cvt_pk_f16_f32 v13, v12, v13
	v_cvt_pk_f16_f32 v12, v10, v11
	v_cvt_pk_f16_f32 v11, v8, v9
	v_cvt_pk_f16_f32 v10, v6, v7
	s_waitcnt lgkmcnt(1)
	v_mfma_f32_16x16x32_f16 v[14:17], v[18:21], v[14:17], 0
	ds_read_b128 v[26:29], v70 offset:2560
	ds_read_b128 v[30:33], v70 offset:2624
	s_load_dwordx2 s[10:11], s[0:1], 0x70
	s_load_dwordx2 s[8:9], s[0:1], 0x98
	s_waitcnt lgkmcnt(0)
	v_mfma_f32_16x16x32_f16 v[6:9], v[10:13], v[22:25], v[14:17]
	v_or_b32_e32 v22, s18, v56
	v_ashrrev_i32_e32 v23, 31, v22
	s_nop 0
	v_lshrrev_b32_e32 v14, 2, v55
	v_or3_b32 v1, s13, v14, v1
	v_mfma_f32_16x16x32_f16 v[18:21], v[18:21], v[26:29], 0
	v_mul_u32_u24_e32 v56, 0x180, v1
	s_nop 0
	v_add_f32_e32 v1, v2, v6
	s_mov_b32 s13, 0xc2200000
	v_mov_b32_e32 v28, 0x42200000
	v_med3_f32 v1, v1, s13, v28
	v_mul_f32_e32 v1, 0x4038aa3b, v1
	v_exp_f32_e32 v6, v1
	v_add_f32_e32 v1, v3, v7
	v_med3_f32 v1, v1, s13, v28
	v_mul_f32_e32 v1, 0x4038aa3b, v1
	v_exp_f32_e32 v7, v1
	v_add_f32_e32 v1, v4, v8
	v_med3_f32 v1, v1, s13, v28
	v_mul_f32_e32 v1, 0x4038aa3b, v1
	v_exp_f32_e32 v8, v1
	v_add_f32_e32 v1, v5, v9
	v_med3_f32 v1, v1, s13, v28
	v_mul_f32_e32 v1, 0x4038aa3b, v1
	v_exp_f32_e32 v9, v1
	v_cvt_f16_f32_e32 v1, v6
	v_lshl_add_u64 v[24:25], v[56:57], 0, v[22:23]
	v_lshl_add_u64 v[14:15], v[24:25], 4, s[10:11]
	global_store_dwordx4 v[14:15], v[6:9], off sc0 sc1
	v_pack_b32_f16 v14, 1.0, v1
	v_cvt_f16_f32_e32 v1, v9
	v_mfma_f32_16x16x32_f16 v[10:13], v[10:13], v[30:33], v[18:21]
	v_mul_f32_e32 v16, v6, v7
	v_mov_b32_e32 v17, v8
	v_pk_mul_f32 v[26:27], v[6:7], v[8:9] op_sel_hi:[1,0]
	v_mov_b32_e32 v20, v9
	v_pk_mul_f32 v[18:19], v[6:7], v[20:21] op_sel_hi:[1,0]
	v_mul_f32_e32 v23, v8, v16
	v_cvt_pk_f16_f32 v15, v7, v16
	v_cvt_pk_f16_f32 v19, v18, v19
	v_pk_mul_f32 v[16:17], v[20:21], v[16:17] op_sel_hi:[0,1]
	v_pk_mul_f32 v[20:21], v[20:21], v[26:27] op_sel_hi:[0,1]
	v_pack_b32_f16 v18, v1, v19
	v_cvt_pk_f16_f32 v1, v16, v17
	v_cvt_pk_f16_f32 v21, v20, v21
	v_alignbit_b32 v19, v1, v19, 16
	v_alignbit_b32 v20, v21, v1, 16
	v_add_f32_e32 v1, v2, v10
	v_med3_f32 v1, v1, s13, v28
	v_mul_f32_e32 v1, 0x4038aa3b, v1
	v_exp_f32_e32 v2, v1
	v_add_f32_e32 v1, v3, v11
	v_med3_f32 v1, v1, s13, v28
	v_mul_f32_e32 v1, 0x4038aa3b, v1
	v_exp_f32_e32 v3, v1
	v_add_f32_e32 v1, v4, v12
	v_med3_f32 v1, v1, s13, v28
	v_mul_f32_e32 v1, 0x4038aa3b, v1
	v_exp_f32_e32 v4, v1
	v_add_f32_e32 v1, v5, v13
	v_lshlrev_b64 v[24:25], 5, v[24:25]
	v_med3_f32 v1, v1, s13, v28
	v_cvt_pk_f16_f32 v16, v8, v26
	v_cvt_pk_f16_f32 v17, v27, v23
	v_lshrrev_b32_e32 v21, 16, v21
	v_lshl_add_u64 v[24:25], s[8:9], 0, v[24:25]
	v_mul_f32_e32 v1, 0x4038aa3b, v1
	v_fma_mixhi_f16 v21, v9, v23, 0
	global_store_dwordx4 v[24:25], v[14:17], off
	global_store_dwordx4 v[24:25], v[18:21], off offset:16
	v_exp_f32_e32 v5, v1
	v_or_b32_e32 v14, 16, v22
	v_cvt_f16_f32_e32 v1, v2
	v_ashrrev_i32_e32 v15, 31, v14
	v_lshl_add_u64 v[18:19], v[56:57], 0, v[14:15]
	v_lshl_add_u64 v[10:11], v[18:19], 4, s[10:11]
	global_store_dwordx4 v[10:11], v[2:5], off sc0 sc1
	v_pack_b32_f16 v10, 1.0, v1
	v_cvt_f16_f32_e32 v1, v5
	v_mov_b32_e32 v16, v5
	v_mul_f32_e32 v12, v2, v3
	v_pk_mul_f32 v[14:15], v[2:3], v[16:17] op_sel_hi:[1,0]
	v_mov_b32_e32 v13, v4
	v_pk_mul_f32 v[20:21], v[2:3], v[4:5] op_sel_hi:[1,0]
	v_mul_f32_e32 v22, v4, v12
	v_cvt_pk_f16_f32 v11, v3, v12
	v_cvt_pk_f16_f32 v15, v14, v15
	v_pk_mul_f32 v[12:13], v[16:17], v[12:13] op_sel_hi:[0,1]
	v_pk_mul_f32 v[16:17], v[16:17], v[20:21] op_sel_hi:[0,1]
	v_pack_b32_f16 v14, v1, v15
	v_cvt_pk_f16_f32 v1, v12, v13
	v_cvt_pk_f16_f32 v17, v16, v17
	v_lshlrev_b64 v[18:19], 5, v[18:19]
	v_alignbit_b32 v15, v1, v15, 16
	v_cvt_pk_f16_f32 v12, v4, v20
	v_cvt_pk_f16_f32 v13, v21, v22
	v_alignbit_b32 v16, v17, v1, 16
	v_lshrrev_b32_e32 v17, 16, v17
	v_lshl_add_u64 v[18:19], s[8:9], 0, v[18:19]
	v_fma_mixhi_f16 v17, v5, v22, 0
	global_store_dwordx4 v[18:19], v[10:13], off
	global_store_dwordx4 v[18:19], v[14:17], off offset:16
	s_and_saveexec_b64 s[8:9], vcc
	s_xor_b64 s[8:9], exec, s[8:9]
	s_cbranch_execz .LBB0_6
	v_mbcnt_lo_u32_b32 v1, -1, 0
	v_mbcnt_hi_u32_b32 v1, -1, v1
	v_and_b32_e32 v10, 64, v1
	v_add_u32_e32 v14, 64, v10
	v_xor_b32_e32 v15, 32, v1
	v_xor_b32_e32 v16, 16, v1
	v_xor_b32_e32 v18, 8, v1
	v_xor_b32_e32 v19, 4, v1
	v_xor_b32_e32 v20, 2, v1
	v_xor_b32_e32 v21, 1, v1

.LBB0_10:
	s_or_b64 exec, exec, s[8:9]
	v_max_f32_e32 v9, v9, v9
	v_max_f32_e32 v8, v8, v8
	v_max_f32_e32 v5, v5, v5
	v_max_f32_e32 v4, v4, v4
	v_max_f32_e32 v8, v8, v9
	v_max_f32_e32 v4, v4, v5
	v_cmp_lt_i32_e32 vcc, v15, v14
	v_max3_f32 v6, v6, v7, v8
	v_max3_f32 v2, v2, v3, v4
	v_cndmask_b32_e32 v3, v1, v15, vcc
	v_max3_f32 v2, v6, 0, v2
	v_lshlrev_b32_e32 v3, 2, v3
	ds_bpermute_b32 v3, v3, v2
	v_cmp_lt_i32_e32 vcc, v16, v14
	s_waitcnt lgkmcnt(0)
	v_max_f32_e32 v3, v3, v3
	v_max_f32_e32 v2, v2, v3
	v_cndmask_b32_e32 v3, v1, v16, vcc
	v_lshlrev_b32_e32 v3, 2, v3
	ds_bpermute_b32 v3, v3, v2
	v_cmp_lt_i32_e32 vcc, v18, v14
	s_waitcnt lgkmcnt(0)
	v_max_f32_e32 v3, v3, v3
	v_max_f32_e32 v2, v2, v3
	v_cndmask_b32_e32 v3, v1, v18, vcc
	v_lshlrev_b32_e32 v3, 2, v3
	ds_bpermute_b32 v3, v3, v2
	v_cmp_lt_i32_e32 vcc, v19, v14
	s_waitcnt lgkmcnt(0)
	v_max_f32_e32 v3, v3, v3
	v_max_f32_e32 v2, v2, v3
	v_cndmask_b32_e32 v3, v1, v19, vcc
	v_lshlrev_b32_e32 v3, 2, v3
	ds_bpermute_b32 v3, v3, v2
	v_cmp_lt_i32_e32 vcc, v20, v14
	s_waitcnt lgkmcnt(0)
	v_max_f32_e32 v3, v3, v3
	v_max_f32_e32 v2, v2, v3
	v_cndmask_b32_e32 v3, v1, v20, vcc
	v_lshlrev_b32_e32 v3, 2, v3
	ds_bpermute_b32 v3, v3, v2
	v_cmp_lt_i32_e32 vcc, v21, v14
	s_waitcnt lgkmcnt(0)
	v_max_f32_e32 v3, v3, v3
	v_cndmask_b32_e32 v1, v1, v21, vcc
	v_max_f32_e32 v2, v2, v3
	v_lshlrev_b32_e32 v1, 2, v1
	ds_bpermute_b32 v1, v1, v2
	v_cmp_eq_u32_e32 vcc, 0, v17
	s_and_saveexec_b64 s[8:9], vcc
	s_cbranch_execz .LBB0_12
	v_lshrrev_b32_e32 v3, 6, v0
	s_waitcnt lgkmcnt(0)
	v_max_f32_e32 v1, v1, v1
	v_max_f32_e32 v2, v2, v2
	v_lshlrev_b32_e32 v3, 2, v3
	v_max_f32_e32 v1, v2, v1
	ds_write_b32 v3, v1 offset:51200
.LBB0_12:
	s_or_b64 exec, exec, s[8:9]
	v_cmp_eq_u32_e32 vcc, 0, v0
	s_waitcnt lgkmcnt(0)
	s_barrier
	s_and_saveexec_b64 s[8:9], vcc
	s_cbranch_execz .LBB0_14
	v_mov_b32_e32 v1, 0
	ds_read_b128 v[2:5], v1 offset:51200
	ds_read_b128 v[6:9], v1 offset:51216
	s_lshl_b32 s10, s12, 3
	s_add_i32 s3, s3, s10
	s_add_i32 s10, s3, 0x80
	s_waitcnt lgkmcnt(1)
	v_max_f32_e32 v3, v3, v3
	v_max_f32_e32 v2, v2, v2
	v_max_f32_e32 v2, v2, v3
	s_mov_b32 s11, 0
	v_max3_f32 v2, v2, v4, v5
	s_lshl_b64 s[10:11], s[10:11], 2
	s_waitcnt lgkmcnt(0)
	v_max3_f32 v2, v2, v6, v7
	s_add_u32 s10, s4, s10
	v_max3_f32 v2, v2, v8, v9
	s_addc_u32 s11, s5, s11
	global_store_dword v1, v2, s[10:11]

.LBB0_16:
	s_andn2_b64 vcc, exec, s[8:9]
	s_cbranch_vccnz .LBB0_27
	v_lshlrev_b32_e32 v24, 2, v0
	v_mov_b32_e32 v25, 0
	v_lshrrev_b32_e32 v1, 2, v0
	s_load_dwordx4 s[12:15], s[0:1], 0x48
	s_load_dwordx4 s[8:11], s[0:1], 0x18
	s_load_dwordx2 s[18:19], s[0:1], 0x0
	v_and_b32_e32 v26, 15, v0
	s_waitcnt lgkmcnt(0)
	v_lshl_add_u64 v[2:3], s[6:7], 0, v[24:25]
	v_lshl_add_u64 v[4:5], s[16:17], 0, v[24:25]
	v_cmp_gt_u32_e32 vcc, 64, v0
	v_and_b32_e32 v18, 48, v1
	v_or_b32_e32 v1, v18, v26
	v_cndmask_b32_e32 v3, v5, v3, vcc
	v_cndmask_b32_e32 v2, v4, v2, vcc
	v_bfe_u32 v23, v0, 4, 2
	global_load_dword v22, v[2:3], off
	v_lshlrev_b32_e32 v2, 8, v1
	v_mov_b32_e32 v3, v25
	v_lshl_add_u64 v[2:3], s[12:13], 0, v[2:3]
	v_lshlrev_b32_e32 v4, 5, v23
	v_mov_b32_e32 v5, v25
	s_lshl_b32 s3, s2, 1
	v_lshl_add_u64 v[10:11], v[2:3], 0, v[4:5]
	s_bfe_u32 s21, s2, 0x10002
	s_lshr_b32 s20, s2, 4
	s_and_b32 s3, s3, 6
	s_bfe_u32 s2, s2, 0x10003
	global_load_dwordx4 v[6:9], v[10:11], off
	v_lshl_add_u64 v[2:3], v[10:11], 0, 16
	s_mov_b64 s[6:7], 0x80
	s_or_b32 s3, s2, s3
	s_lshl_b32 s2, s20, 6
	s_mul_i32 s22, s21, 0x180
	global_load_dwordx4 v[14:17], v[2:3], off
	v_lshl_add_u64 v[2:3], v[10:11], 0, s[6:7]
	s_mov_b64 s[6:7], 0x90
	s_add_i32 s22, s22, s2
	s_lshl_b32 s21, s21, 3
	v_lshl_add_u64 v[10:11], v[10:11], 0, s[6:7]
	v_lshlrev_b32_e32 v28, 2, v18
	v_mov_b32_e32 v29, v25
	s_lshl_b32 s6, s3, 8
	global_load_dwordx4 v[2:5], v[2:3], off
	v_lshl_add_u64 v[30:31], s[14:15], 0, v[28:29]
	v_and_b32_e32 v64, 48, v0
	v_mov_b32_e32 v65, v25
	s_add_u32 s6, s10, s6
	global_load_dwordx4 v[10:13], v[10:11], off
	v_lshl_add_u64 v[18:19], v[30:31], 0, v[64:65]
	s_addc_u32 s7, s11, 0
	global_load_dwordx4 v[18:21], v[18:19], off
	v_lshlrev_b32_e32 v32, 2, v26
	v_mov_b32_e32 v33, v25
	v_lshl_add_u64 v[28:29], s[6:7], 0, v[28:29]
	v_lshrrev_b32_e32 v60, 4, v0
	v_lshl_add_u64 v[30:31], v[30:31], 0, v[32:33]
	global_load_dword v96, v[30:31], off
	v_lshl_add_u64 v[28:29], v[28:29], 0, v[32:33]
	v_or_b32_e32 v27, s22, v60
	global_load_dword v97, v[28:29], off
	v_lshlrev_b32_e32 v28, 11, v27
	v_mov_b32_e32 v29, v25
	v_and_b32_e32 v61, 60, v24
	v_lshl_add_u64 v[28:29], s[18:19], 0, v[28:29]
	v_lshlrev_b32_e32 v24, 2, v61
	v_lshl_add_u64 v[88:89], v[28:29], 0, v[24:25]
	global_load_dwordx4 v[28:31], v[88:89], off
	s_mov_b32 s6, 0x10000
	v_add_co_u32_e32 v90, vcc, s6, v88
	v_lshlrev_b32_e32 v27, 9, v60
	s_nop 0
	v_addc_co_u32_e32 v91, vcc, 0, v89, vcc
	global_load_dwordx4 v[32:35], v[90:91], off
	v_lshl_or_b32 v36, s3, 15, v27
	v_mov_b32_e32 v37, v25
	v_lshl_add_u64 v[36:37], v[36:37], 2, s[8:9]
	v_lshl_add_u64 v[92:93], v[36:37], 0, v[24:25]
	global_load_dwordx4 v[36:39], v[92:93], off
	v_add_co_u32_e32 v94, vcc, s6, v92
	v_lshrrev_b32_e32 v24, 3, v0
	s_nop 0
	v_addc_co_u32_e32 v95, vcc, 0, v93, vcc
	global_load_dwordx4 v[40:43], v[94:95], off
	global_load_dwordx4 v[44:47], v[88:89], off offset:256
	global_load_dwordx4 v[48:51], v[90:91], off offset:256
	global_load_dwordx4 v[52:55], v[92:93], off offset:256
	global_load_dwordx4 v[56:59], v[94:95], off offset:256
	v_and_b32_e32 v24, 32, v24
	v_or_b32_e32 v62, v24, v26
	s_movk_i32 s6, 0xa0
	v_mad_u32_u24 v99, v62, s6, v64
	v_mad_u32_u24 v100, v1, s6, v64
	v_lshlrev_b32_e32 v23, 2, v23
	s_load_dwordx2 s[0:1], s[0:1], 0x68
	s_or_b32 s6, s3, s21
	v_cmp_lt_u32_e32 vcc, 63, v0
	s_waitcnt vmcnt(7)
	v_cvt_f16_f32_e32 v27, v28
	v_cvt_f16_f32_e32 v28, v31
	v_cvt_pk_f16_f32 v29, v29, v30
	v_pack_b32_f16 v26, v27, v29
	v_alignbit_b32 v27, v28, v29, 16
	v_mul_u32_u24_e32 v28, 0xa0, v60
	s_waitcnt vmcnt(6)
	v_cvt_f16_f32_e32 v29, v32
	v_cvt_f16_f32_e32 v30, v35
	v_cvt_pk_f16_f32 v31, v33, v34
	v_lshl_add_u32 v98, v61, 1, v28
	v_pack_b32_f16 v28, v29, v31
	v_alignbit_b32 v29, v30, v31, 16
	s_waitcnt vmcnt(5)
	v_cvt_f16_f32_e32 v30, v36
	ds_write2st64_b64 v98, v[26:27], v[28:29] offset1:10
	v_cvt_pk_f16_f32 v27, v37, v38
	v_cvt_f16_f32_e32 v28, v39
	v_pack_b32_f16 v26, v30, v27
	s_waitcnt vmcnt(4)
	v_cvt_f16_f32_e32 v29, v40
	v_cvt_f16_f32_e32 v30, v43
	v_cvt_pk_f16_f32 v31, v41, v42
	v_alignbit_b32 v27, v28, v27, 16
	v_pack_b32_f16 v28, v29, v31
	v_alignbit_b32 v29, v30, v31, 16
	ds_write2st64_b64 v98, v[26:27], v[28:29] offset0:60 offset1:70
	global_load_dwordx4 v[26:29], v[88:89], off offset:512
	global_load_dwordx4 v[30:33], v[90:91], off offset:512
	global_load_dwordx4 v[34:37], v[92:93], off offset:512
	global_load_dwordx4 v[38:41], v[94:95], off offset:512
	s_waitcnt vmcnt(7)
	v_cvt_f16_f32_e32 v42, v44
	v_cvt_pk_f16_f32 v43, v45, v46
	v_cvt_f16_f32_e32 v44, v47
	s_waitcnt vmcnt(6)
	v_cvt_f16_f32_e32 v45, v48
	v_cvt_f16_f32_e32 v47, v51
	v_cvt_pk_f16_f32 v46, v49, v50
	s_waitcnt vmcnt(5)
	v_cvt_f16_f32_e32 v48, v52
	v_cvt_pk_f16_f32 v49, v53, v54
	v_cvt_f16_f32_e32 v50, v55
	s_waitcnt vmcnt(4)
	v_cvt_f16_f32_e32 v51, v56
	v_cvt_f16_f32_e32 v53, v59
	v_cvt_pk_f16_f32 v52, v57, v58
	v_pack_b32_f16 v42, v42, v43
	v_alignbit_b32 v43, v44, v43, 16
	v_pack_b32_f16 v44, v45, v46
	v_alignbit_b32 v45, v47, v46, 16
	s_waitcnt lgkmcnt(0)
	s_barrier
	ds_read_b128 v[60:63], v99
	ds_read_b128 v[64:67], v100 offset:30720
	ds_read_b128 v[68:71], v99 offset:64
	ds_read_b128 v[72:75], v100 offset:30784
	ds_read_b128 v[76:79], v99 offset:2560
	ds_read_b128 v[80:83], v99 offset:2624
	v_pack_b32_f16 v46, v48, v49
	v_alignbit_b32 v47, v50, v49, 16
	v_pack_b32_f16 v48, v51, v52
	v_alignbit_b32 v49, v53, v52, 16
	ds_write2st64_b64 v98, v[42:43], v[44:45] offset0:20 offset1:30
	ds_write2st64_b64 v98, v[46:47], v[48:49] offset0:80 offset1:90
	global_load_dwordx4 v[42:45], v[88:89], off offset:768
	global_load_dwordx4 v[46:49], v[90:91], off offset:768
	global_load_dwordx4 v[50:53], v[92:93], off offset:768
	global_load_dwordx4 v[54:57], v[94:95], off offset:768
	s_waitcnt lgkmcnt(6)
	v_mfma_f32_16x16x32_f16 v[60:63], v[60:63], v[64:67], 0
	s_waitcnt lgkmcnt(0)
	s_barrier
	v_mfma_f32_16x16x32_f16 v[60:63], v[68:71], v[72:75], v[60:63]
	ds_read_b128 v[68:71], v99 offset:10240
	s_waitcnt vmcnt(7)
	v_cvt_f16_f32_e32 v26, v26
	v_mfma_f32_16x16x32_f16 v[64:67], v[76:79], v[64:67], 0
	v_cvt_pk_f16_f32 v27, v27, v28
	v_cvt_f16_f32_e32 v28, v29
	s_waitcnt vmcnt(6)
	v_cvt_f16_f32_e32 v29, v30
	v_cvt_pk_f16_f32 v30, v31, v32
	v_cvt_f16_f32_e32 v31, v33
	s_waitcnt vmcnt(5)
	v_cvt_f16_f32_e32 v32, v34
	v_cvt_pk_f16_f32 v33, v35, v36
	v_cvt_f16_f32_e32 v34, v37
	s_waitcnt vmcnt(4)
	v_cvt_f16_f32_e32 v35, v38
	v_cvt_f16_f32_e32 v37, v41
	v_mfma_f32_16x16x32_f16 v[64:67], v[80:83], v[72:75], v[64:67]
	ds_read_b128 v[72:75], v100 offset:40960
	ds_read_b128 v[76:79], v99 offset:10304
	ds_read_b128 v[80:83], v100 offset:41024
	v_cvt_pk_f16_f32 v36, v39, v40
	v_pack_b32_f16 v26, v26, v27
	v_alignbit_b32 v27, v28, v27, 16
	v_pack_b32_f16 v28, v29, v30
	v_alignbit_b32 v29, v31, v30, 16
	s_waitcnt lgkmcnt(2)
	v_mfma_f32_16x16x32_f16 v[58:61], v[68:71], v[72:75], v[60:63]
	ds_read_b128 v[68:71], v99 offset:12800
	ds_read_b128 v[84:87], v99 offset:12864
	v_pack_b32_f16 v30, v32, v33
	v_alignbit_b32 v31, v34, v33, 16
	v_pack_b32_f16 v32, v35, v36
	v_alignbit_b32 v33, v37, v36, 16
	ds_write2st64_b64 v98, v[26:27], v[28:29] offset1:10
	ds_write2st64_b64 v98, v[30:31], v[32:33] offset0:60 offset1:70
	global_load_dwordx4 v[26:29], v[88:89], off offset:1024
	global_load_dwordx4 v[30:33], v[90:91], off offset:1024
	global_load_dwordx4 v[34:37], v[92:93], off offset:1024
	global_load_dwordx4 v[38:41], v[94:95], off offset:1024
	s_waitcnt lgkmcnt(3)
	v_mfma_f32_16x16x32_f16 v[62:65], v[68:71], v[72:75], v[64:67]
	s_waitcnt lgkmcnt(0)
	s_barrier
	s_nop 0
	ds_read_b128 v[66:69], v99
	s_waitcnt vmcnt(7)
	v_cvt_f16_f32_e32 v42, v42
	v_cvt_pk_f16_f32 v43, v43, v44
	v_cvt_f16_f32_e32 v44, v45
	s_waitcnt vmcnt(6)
	v_cvt_f16_f32_e32 v45, v46
	v_cvt_pk_f16_f32 v46, v47, v48
	v_cvt_f16_f32_e32 v47, v49
	v_mfma_f32_16x16x32_f16 v[58:61], v[76:79], v[80:83], v[58:61]
	s_waitcnt vmcnt(5)
	v_cvt_f16_f32_e32 v48, v50
	v_cvt_pk_f16_f32 v49, v51, v52
	v_cvt_f16_f32_e32 v50, v53
	s_waitcnt vmcnt(4)
	v_cvt_f16_f32_e32 v51, v54
	v_cvt_f16_f32_e32 v53, v57
	v_mfma_f32_16x16x32_f16 v[62:65], v[84:87], v[80:83], v[62:65]
	ds_read_b128 v[70:73], v100 offset:30720
	ds_read_b128 v[74:77], v99 offset:64
	ds_read_b128 v[78:81], v100 offset:30784
	v_cvt_pk_f16_f32 v52, v55, v56
	v_pack_b32_f16 v42, v42, v43
	v_alignbit_b32 v43, v44, v43, 16
	v_pack_b32_f16 v44, v45, v46
	v_alignbit_b32 v45, v47, v46, 16
	s_waitcnt lgkmcnt(2)
	v_mfma_f32_16x16x32_f16 v[58:61], v[66:69], v[70:73], v[58:61]
	ds_read_b128 v[66:69], v99 offset:2560
	ds_read_b128 v[82:85], v99 offset:2624
	v_pack_b32_f16 v46, v48, v49
	v_alignbit_b32 v47, v50, v49, 16
	v_pack_b32_f16 v48, v51, v52
	v_alignbit_b32 v49, v53, v52, 16
	ds_write2st64_b64 v98, v[42:43], v[44:45] offset0:20 offset1:30
	ds_write2st64_b64 v98, v[46:47], v[48:49] offset0:80 offset1:90
	global_load_dwordx4 v[42:45], v[88:89], off offset:1280
	global_load_dwordx4 v[46:49], v[90:91], off offset:1280
	global_load_dwordx4 v[50:53], v[92:93], off offset:1280
	global_load_dwordx4 v[54:57], v[94:95], off offset:1280
	s_waitcnt lgkmcnt(3)
	v_mfma_f32_16x16x32_f16 v[62:65], v[66:69], v[70:73], v[62:65]
	s_waitcnt lgkmcnt(0)
	s_barrier
	ds_read_b128 v[66:69], v99 offset:10240
	v_mfma_f32_16x16x32_f16 v[58:61], v[74:77], v[78:81], v[58:61]
	s_waitcnt vmcnt(7)
	v_cvt_f16_f32_e32 v26, v26
	v_mfma_f32_16x16x32_f16 v[62:65], v[82:85], v[78:81], v[62:65]
	ds_read_b128 v[70:73], v100 offset:40960
	ds_read_b128 v[74:77], v99 offset:10304
	ds_read_b128 v[78:81], v100 offset:41024
	v_cvt_pk_f16_f32 v27, v27, v28
	v_cvt_f16_f32_e32 v28, v29
	s_waitcnt vmcnt(6)
	v_cvt_f16_f32_e32 v29, v30
	v_cvt_pk_f16_f32 v30, v31, v32
	v_cvt_f16_f32_e32 v31, v33
	s_waitcnt vmcnt(5)
	v_cvt_f16_f32_e32 v32, v34
	v_cvt_pk_f16_f32 v33, v35, v36
	v_cvt_f16_f32_e32 v34, v37
	s_waitcnt vmcnt(4)
	v_cvt_f16_f32_e32 v35, v38
	v_cvt_f16_f32_e32 v37, v41
	s_waitcnt lgkmcnt(2)
	v_mfma_f32_16x16x32_f16 v[58:61], v[66:69], v[70:73], v[58:61]
	ds_read_b128 v[66:69], v99 offset:12800
	ds_read_b128 v[82:85], v99 offset:12864
	v_cvt_pk_f16_f32 v36, v39, v40
	v_pack_b32_f16 v26, v26, v27
	v_alignbit_b32 v27, v28, v27, 16
	v_pack_b32_f16 v28, v29, v30
	v_alignbit_b32 v29, v31, v30, 16
	v_pack_b32_f16 v30, v32, v33
	v_alignbit_b32 v31, v34, v33, 16
	v_pack_b32_f16 v32, v35, v36
	v_alignbit_b32 v33, v37, v36, 16
	ds_write2st64_b64 v98, v[26:27], v[28:29] offset1:10
	ds_write2st64_b64 v98, v[30:31], v[32:33] offset0:60 offset1:70
	s_waitcnt lgkmcnt(3)
	v_mfma_f32_16x16x32_f16 v[62:65], v[66:69], v[70:73], v[62:65]
	global_load_dwordx4 v[26:29], v[88:89], off offset:1536
	global_load_dwordx4 v[30:33], v[90:91], off offset:1536
	global_load_dwordx4 v[34:37], v[92:93], off offset:1536
	global_load_dwordx4 v[38:41], v[94:95], off offset:1536
	s_waitcnt lgkmcnt(0)
	s_barrier
	ds_read_b128 v[66:69], v99
	v_mfma_f32_16x16x32_f16 v[58:61], v[74:77], v[78:81], v[58:61]
	s_waitcnt vmcnt(6)
	v_cvt_f16_f32_e32 v49, v49
	s_waitcnt vmcnt(5)
	v_cvt_f16_f32_e32 v50, v50
	v_mfma_f32_16x16x32_f16 v[62:65], v[82:85], v[78:81], v[62:65]
	ds_read_b128 v[70:73], v100 offset:30720
	ds_read_b128 v[74:77], v99 offset:64
	ds_read_b128 v[78:81], v100 offset:30784
	global_load_dwordx4 v[82:85], v[88:89], off offset:1792
	ds_read_b128 v[86:89], v99 offset:2624
	s_waitcnt lgkmcnt(3)
	v_mfma_f32_16x16x32_f16 v[58:61], v[66:69], v[70:73], v[58:61]
	ds_read_b128 v[66:69], v99 offset:2560
	v_cvt_pk_f16_f32 v51, v51, v52
	v_cvt_f16_f32_e32 v52, v53
	s_waitcnt lgkmcnt(0)
	v_mfma_f32_16x16x32_f16 v[62:65], v[66:69], v[70:73], v[62:65]
	global_load_dwordx4 v[66:69], v[90:91], off offset:1792
	v_cvt_f16_f32_e32 v70, v42
	v_cvt_f16_f32_e32 v72, v45
	v_cvt_f16_f32_e32 v73, v46
	v_mfma_f32_16x16x32_f16 v[58:61], v[74:77], v[78:81], v[58:61]
	v_cvt_pk_f16_f32 v71, v43, v44
	v_cvt_pk_f16_f32 v74, v47, v48
	global_load_dwordx4 v[42:45], v[92:93], off offset:1792
	v_pack_b32_f16 v46, v70, v71
	v_alignbit_b32 v47, v72, v71, 16
	v_pack_b32_f16 v48, v73, v74
	v_alignbit_b32 v49, v49, v74, 16
	ds_write2st64_b64 v98, v[46:47], v[48:49] offset0:20 offset1:30
	global_load_dwordx4 v[46:49], v[94:95], off offset:1792
	s_waitcnt vmcnt(8)
	v_cvt_f16_f32_e32 v53, v54
	v_cvt_pk_f16_f32 v54, v55, v56
	v_cvt_f16_f32_e32 v55, v57
	v_pack_b32_f16 v50, v50, v51
	v_alignbit_b32 v51, v52, v51, 16
	v_pack_b32_f16 v52, v53, v54
	v_alignbit_b32 v53, v55, v54, 16
	ds_write2st64_b64 v98, v[50:51], v[52:53] offset0:80 offset1:90
	s_waitcnt lgkmcnt(0)
	s_barrier
	ds_read_b128 v[50:53], v99 offset:10240
	v_mfma_f32_16x16x32_f16 v[54:57], v[86:89], v[78:81], v[62:65]
	s_nop 2
	ds_read_b128 v[62:65], v100 offset:40960
	ds_read_b128 v[70:73], v99 offset:10304
	ds_read_b128 v[74:77], v100 offset:41024
	s_waitcnt vmcnt(7)
	v_cvt_f16_f32_e32 v26, v26
	v_cvt_pk_f16_f32 v27, v27, v28
	v_cvt_f16_f32_e32 v28, v29
	s_waitcnt vmcnt(6)
	v_cvt_f16_f32_e32 v29, v30
	v_cvt_pk_f16_f32 v30, v31, v32
	v_cvt_f16_f32_e32 v31, v33
	s_waitcnt vmcnt(5)
	v_cvt_f16_f32_e32 v32, v34
	v_cvt_pk_f16_f32 v33, v35, v36
	v_cvt_f16_f32_e32 v34, v37
	s_waitcnt vmcnt(4)
	v_cvt_f16_f32_e32 v35, v38
	v_cvt_f16_f32_e32 v37, v41
	s_waitcnt lgkmcnt(2)
	v_mfma_f32_16x16x32_f16 v[50:53], v[50:53], v[62:65], v[58:61]
	s_nop 2
	ds_read_b128 v[58:61], v99 offset:12800
	ds_read_b128 v[78:81], v99 offset:12864
	v_cvt_pk_f16_f32 v36, v39, v40
	v_pack_b32_f16 v26, v26, v27
	v_alignbit_b32 v27, v28, v27, 16
	v_pack_b32_f16 v28, v29, v30
	v_alignbit_b32 v29, v31, v30, 16
	s_waitcnt vmcnt(3)
	v_cvt_f16_f32_e32 v38, v82
	v_cvt_f16_f32_e32 v40, v85
	v_pack_b32_f16 v30, v32, v33
	v_alignbit_b32 v31, v34, v33, 16
	v_pack_b32_f16 v32, v35, v36
	v_alignbit_b32 v33, v37, v36, 16
	ds_write2st64_b64 v98, v[26:27], v[28:29] offset1:10
	ds_write2st64_b64 v98, v[30:31], v[32:33] offset0:60 offset1:70
	s_waitcnt lgkmcnt(0)
	s_barrier
	s_waitcnt vmcnt(2)
	v_cvt_f16_f32_e32 v41, v66
	ds_read_b128 v[26:29], v99
	v_mfma_f32_16x16x32_f16 v[54:57], v[58:61], v[62:65], v[54:57]
	v_cvt_pk_f16_f32 v39, v83, v84
	v_cvt_pk_f16_f32 v58, v67, v68
	v_pack_b32_f16 v62, v38, v39
	v_alignbit_b32 v63, v40, v39, 16
	v_pack_b32_f16 v64, v41, v58
	ds_read_b128 v[34:37], v99 offset:2560
	ds_read_b128 v[38:41], v100 offset:30720
	v_mfma_f32_16x16x32_f16 v[30:33], v[70:73], v[74:77], v[50:53]
	v_cvt_f16_f32_e32 v59, v69
	s_waitcnt vmcnt(1)
	v_cvt_f16_f32_e32 v42, v42
	v_cvt_pk_f16_f32 v43, v43, v44
	v_mfma_f32_16x16x32_f16 v[50:53], v[78:81], v[74:77], v[54:57]
	v_cvt_f16_f32_e32 v44, v45
	v_alignbit_b32 v65, v59, v58, 16
	s_nop 0
	ds_read_b128 v[54:57], v99 offset:64
	ds_read_b128 v[58:61], v100 offset:30784
	s_waitcnt lgkmcnt(2)
	v_mfma_f32_16x16x32_f16 v[26:29], v[26:29], v[38:41], v[30:33]
	v_mfma_f32_16x16x32_f16 v[34:37], v[34:37], v[38:41], v[50:53]
	s_waitcnt vmcnt(0)
	v_cvt_f16_f32_e32 v40, v46
	v_cvt_f16_f32_e32 v41, v49
	ds_read_b128 v[30:33], v99 offset:2624
	v_pack_b32_f16 v38, v42, v43
	v_cvt_pk_f16_f32 v42, v47, v48
	v_alignbit_b32 v39, v44, v43, 16
	v_pack_b32_f16 v40, v40, v42
	v_alignbit_b32 v41, v41, v42, 16
	ds_write2st64_b64 v98, v[62:63], v[64:65] offset0:20 offset1:30
	ds_write2st64_b64 v98, v[38:39], v[40:41] offset0:80 offset1:90
	s_waitcnt lgkmcnt(0)
	s_barrier
	ds_read_b128 v[38:41], v99 offset:10240
	v_mfma_f32_16x16x32_f16 v[26:29], v[54:57], v[58:61], v[26:29]
	v_mfma_f32_16x16x32_f16 v[30:33], v[30:33], v[58:61], v[34:37]
	s_nop 2
	ds_read_b128 v[34:37], v100 offset:40960
	ds_read_b128 v[42:45], v99 offset:10304
	ds_read_b128 v[46:49], v100 offset:41024
	s_waitcnt lgkmcnt(2)
	v_mfma_f32_16x16x32_f16 v[26:29], v[38:41], v[34:37], v[26:29]
	ds_read_b128 v[38:41], v99 offset:12800
	ds_read_b128 v[50:53], v99 offset:12864
	s_waitcnt vmcnt(0)
	s_waitcnt lgkmcnt(0)
	v_mfma_f32_16x16x32_f16 v[26:29], v[42:45], v[46:49], v[26:29]
	v_or_b32_e32 v18, v23, v24
	v_mul_u32_u24_e32 v18, 0xa0, v18
	v_lshl_add_u32 v18, v1, 1, v18
	v_mfma_f32_16x16x32_f16 v[30:33], v[38:41], v[34:37], v[30:33]
	s_barrier
	s_nop 2
	v_add_f32_e32 v19, v26, v97
	v_cvt_f16_f32_e32 v19, v19
	v_mfma_f32_16x16x32_f16 v[30:33], v[50:53], v[46:49], v[30:33]
	v_add_f32_e32 v20, v27, v97
	v_cvt_f16_f32_e32 v20, v20
	v_add_f32_e32 v21, v28, v97
	v_cvt_f16_f32_e32 v21, v21
	v_add_f32_e32 v26, v29, v97
	v_cvt_f16_f32_e32 v26, v26
	ds_write_b16 v18, v19
	ds_write_b16 v18, v20 offset:160
	ds_write_b16 v18, v21 offset:320
	ds_write_b16 v18, v26 offset:480
	v_add_f32_e32 v19, v30, v97
	v_cvt_f16_f32_e32 v19, v19
	v_add_f32_e32 v20, v31, v97
	v_cvt_f16_f32_e32 v20, v20
	v_add_f32_e32 v21, v32, v97
	v_cvt_f16_f32_e32 v21, v21
	v_add_f32_e32 v26, v33, v97
	v_cvt_f16_f32_e32 v26, v26
	ds_write_b16 v18, v19 offset:2560
	ds_write_b16 v18, v20 offset:2720
	ds_write_b16 v18, v21 offset:2880
	ds_write_b16 v18, v26 offset:3040
	s_waitcnt lgkmcnt(0)
	s_barrier
	ds_read_b128 v[18:21], v99
	v_cvt_pk_f16_f32 v17, v16, v17
	v_cvt_pk_f16_f32 v16, v14, v15
	v_cvt_pk_f16_f32 v15, v8, v9
	v_cvt_pk_f16_f32 v14, v6, v7
	ds_read_b128 v[6:9], v99 offset:64
	ds_read_b128 v[26:29], v99 offset:2560
	ds_read_b128 v[30:33], v99 offset:2624
	s_waitcnt lgkmcnt(3)
	v_mfma_f32_16x16x32_f16 v[18:21], v[18:21], v[14:17], 0
	v_cvt_pk_f16_f32 v13, v12, v13
	v_cvt_pk_f16_f32 v12, v10, v11
	v_cvt_pk_f16_f32 v11, v4, v5
	s_waitcnt lgkmcnt(1)
	v_mfma_f32_16x16x32_f16 v[14:17], v[26:29], v[14:17], 0
	v_cvt_pk_f16_f32 v10, v2, v3
	s_nop 1
	v_mfma_f32_16x16x32_f16 v[2:5], v[6:9], v[10:13], v[18:21]
	s_waitcnt lgkmcnt(0)
	v_mfma_f32_16x16x32_f16 v[6:9], v[30:33], v[10:13], v[14:17]
	v_or3_b32 v12, s2, v24, v23
	v_lshlrev_b32_e32 v24, 3, v1
	v_lshl_add_u64 v[10:11], s[0:1], 0, v[24:25]
	s_nop 2
	v_add_f32_e32 v1, v96, v2
	s_mov_b32 s0, 0xc2200000
	v_mov_b32_e32 v14, 0x42200000
	v_med3_f32 v1, v1, s0, v14
	v_mul_f32_e32 v1, 0x4038aa3b, v1
	v_exp_f32_e32 v2, v1
	v_add_f32_e32 v1, v96, v3
	v_med3_f32 v1, v1, s0, v14
	v_mul_f32_e32 v1, 0x4038aa3b, v1
	s_mul_i32 s2, s6, 0xc0
	v_exp_f32_e32 v3, v1
	v_lshrrev_b32_e32 v1, 1, v12
	v_add_u32_e32 v24, s2, v1
	v_add_f32_e32 v1, v96, v4
	v_med3_f32 v1, v1, s0, v14
	v_mul_f32_e32 v1, 0x4038aa3b, v1
	v_exp_f32_e32 v4, v1
	v_add_f32_e32 v1, v96, v5
	v_med3_f32 v1, v1, s0, v14
	v_mul_f32_e32 v1, 0x4038aa3b, v1
	v_exp_f32_e32 v5, v1
	v_add_f32_e32 v1, v96, v6
	v_med3_f32 v1, v1, s0, v14
	v_mul_f32_e32 v1, 0x4038aa3b, v1
	v_exp_f32_e32 v6, v1
	v_add_f32_e32 v1, v96, v7
	v_med3_f32 v1, v1, s0, v14
	v_mul_f32_e32 v1, 0x4038aa3b, v1
	v_lshlrev_b64 v[12:13], 9, v[24:25]
	v_exp_f32_e32 v7, v1
	v_add_f32_e32 v1, v96, v8
	v_lshl_add_u64 v[12:13], v[10:11], 0, v[12:13]
	v_med3_f32 v1, v1, s0, v14
	global_store_dwordx2 v[12:13], v[2:3], off
	v_or_b32_e32 v12, 1, v24
	v_mov_b32_e32 v13, v25
	v_mul_f32_e32 v1, 0x4038aa3b, v1
	v_lshlrev_b64 v[12:13], 9, v[12:13]
	v_exp_f32_e32 v8, v1
	v_add_f32_e32 v1, v96, v9
	v_lshl_add_u64 v[12:13], v[10:11], 0, v[12:13]
	v_med3_f32 v1, v1, s0, v14
	global_store_dwordx2 v[12:13], v[4:5], off
	v_or_b32_e32 v12, 8, v24
	v_mov_b32_e32 v13, v25
	v_mul_f32_e32 v1, 0x4038aa3b, v1
	v_lshlrev_b64 v[12:13], 9, v[12:13]
	v_exp_f32_e32 v9, v1
	v_lshl_add_u64 v[12:13], v[10:11], 0, v[12:13]
	v_or_b32_e32 v24, 9, v24
	global_store_dwordx2 v[12:13], v[6:7], off
	v_lshlrev_b64 v[12:13], 9, v[24:25]
	v_lshl_add_u64 v[10:11], v[10:11], 0, v[12:13]
	global_store_dwordx2 v[10:11], v[8:9], off
	v_mbcnt_lo_u32_b32 v10, -1, 0
	s_and_saveexec_b64 s[0:1], vcc
	s_xor_b64 s[0:1], exec, s[0:1]
	v_mbcnt_hi_u32_b32 v1, -1, v10
	v_and_b32_e32 v10, 64, v1
	v_add_u32_e32 v14, 64, v10
	v_xor_b32_e32 v15, 32, v1
	v_xor_b32_e32 v16, 16, v1
	v_xor_b32_e32 v18, 8, v1
	v_xor_b32_e32 v19, 4, v1
	v_xor_b32_e32 v20, 2, v1
	v_xor_b32_e32 v21, 1, v1
	s_or_saveexec_b64 s[0:1], s[0:1]
	v_and_b32_e32 v17, 63, v0
	s_xor_b64 exec, exec, s[0:1]
	s_cbranch_execz .LBB0_23
	v_mbcnt_hi_u32_b32 v1, -1, v10
	v_and_b32_e32 v10, 64, v1
	v_add_u32_e32 v14, 64, v10
	v_xor_b32_e32 v15, 32, v1
	v_cmp_lt_i32_e32 vcc, v15, v14
	v_and_b32_e32 v23, 0x7fffffff, v22
	v_xor_b32_e32 v16, 16, v1
	v_cndmask_b32_e32 v10, v1, v15, vcc
	v_lshlrev_b32_e32 v11, 2, v10
	ds_bpermute_b32 v10, v11, v22
	ds_bpermute_b32 v11, v11, v23
	v_cmp_lt_i32_e32 vcc, v16, v14
	v_xor_b32_e32 v18, 8, v1
	s_waitcnt lgkmcnt(0)
	v_pk_add_f32 v[10:11], v[22:23], v[10:11]
	v_cndmask_b32_e32 v12, v1, v16, vcc
	v_lshlrev_b32_e32 v13, 2, v12
	ds_bpermute_b32 v12, v13, v10
	ds_bpermute_b32 v13, v13, v11
	v_cmp_lt_i32_e32 vcc, v18, v14
	s_waitcnt lgkmcnt(0)
	v_pk_add_f32 v[10:11], v[10:11], v[12:13]
	v_cndmask_b32_e32 v19, v1, v18, vcc
	v_lshlrev_b32_e32 v19, 2, v19
	ds_bpermute_b32 v12, v19, v10
	ds_bpermute_b32 v13, v19, v11
	v_xor_b32_e32 v19, 4, v1
	v_cmp_lt_i32_e32 vcc, v19, v14
	s_waitcnt lgkmcnt(0)
	v_pk_add_f32 v[10:11], v[10:11], v[12:13]
	v_cndmask_b32_e32 v20, v1, v19, vcc
	v_lshlrev_b32_e32 v20, 2, v20
	ds_bpermute_b32 v12, v20, v10
	ds_bpermute_b32 v13, v20, v11
	v_xor_b32_e32 v20, 2, v1
	v_cmp_lt_i32_e32 vcc, v20, v14
	s_waitcnt lgkmcnt(0)
	v_pk_add_f32 v[10:11], v[10:11], v[12:13]
	v_cndmask_b32_e32 v21, v1, v20, vcc
	v_lshlrev_b32_e32 v21, 2, v21
	ds_bpermute_b32 v12, v21, v10
	ds_bpermute_b32 v13, v21, v11
	v_xor_b32_e32 v21, 1, v1
	v_cmp_lt_i32_e32 vcc, v21, v14
	s_waitcnt lgkmcnt(0)
	v_pk_add_f32 v[10:11], v[10:11], v[12:13]
	v_cndmask_b32_e32 v12, v1, v21, vcc
	v_lshlrev_b32_e32 v13, 2, v12
	ds_bpermute_b32 v12, v13, v10
	ds_bpermute_b32 v13, v13, v11
	v_cmp_eq_u32_e32 vcc, 0, v17
	s_and_saveexec_b64 s[2:3], vcc
	s_cbranch_execz .LBB0_22
	v_mov_b32_e32 v22, 0
	s_waitcnt lgkmcnt(0)
	v_pk_add_f32 v[10:11], v[10:11], v[12:13]
	global_store_dwordx2 v22, v[10:11], s[4:5] offset:1024

.LBB0_23:
	s_or_b64 exec, exec, s[0:1]
	v_max_f32_e32 v3, v3, v3
	v_max_f32_e32 v2, v2, v2
	v_max_f32_e32 v2, v2, v3
	v_max_f32_e32 v3, v5, v5
	v_max_f32_e32 v4, v4, v4
	v_max_f32_e32 v3, v4, v3
	v_max3_f32 v2, v2, 0, v3
	v_max_f32_e32 v3, v7, v7
	v_max_f32_e32 v4, v6, v6
	v_max_f32_e32 v3, v4, v3
	v_max_f32_e32 v4, v9, v9
	v_max_f32_e32 v5, v8, v8
	v_max_f32_e32 v4, v5, v4
	v_cmp_lt_i32_e32 vcc, v15, v14
	v_max3_f32 v2, v2, v3, v4
	s_nop 0
	v_cndmask_b32_e32 v3, v1, v15, vcc
	v_lshlrev_b32_e32 v3, 2, v3
	ds_bpermute_b32 v3, v3, v2
	v_cmp_lt_i32_e32 vcc, v16, v14
	s_waitcnt lgkmcnt(0)
	v_max_f32_e32 v3, v3, v3
	v_max_f32_e32 v2, v2, v3
	v_cndmask_b32_e32 v3, v1, v16, vcc
	v_lshlrev_b32_e32 v3, 2, v3
	ds_bpermute_b32 v3, v3, v2
	v_cmp_lt_i32_e32 vcc, v18, v14
	s_waitcnt lgkmcnt(0)
	v_max_f32_e32 v3, v3, v3
	v_max_f32_e32 v2, v2, v3
	v_cndmask_b32_e32 v3, v1, v18, vcc
	v_lshlrev_b32_e32 v3, 2, v3
	ds_bpermute_b32 v3, v3, v2
	v_cmp_lt_i32_e32 vcc, v19, v14
	s_waitcnt lgkmcnt(0)
	v_max_f32_e32 v3, v3, v3
	v_max_f32_e32 v2, v2, v3
	v_cndmask_b32_e32 v3, v1, v19, vcc
	v_lshlrev_b32_e32 v3, 2, v3
	ds_bpermute_b32 v3, v3, v2
	v_cmp_lt_i32_e32 vcc, v20, v14
	s_waitcnt lgkmcnt(0)
	v_max_f32_e32 v3, v3, v3
	v_max_f32_e32 v2, v2, v3
	v_cndmask_b32_e32 v3, v1, v20, vcc
	v_lshlrev_b32_e32 v3, 2, v3
	ds_bpermute_b32 v3, v3, v2
	v_cmp_lt_i32_e32 vcc, v21, v14
	s_waitcnt lgkmcnt(0)
	v_max_f32_e32 v3, v3, v3
	v_cndmask_b32_e32 v1, v1, v21, vcc
	v_max_f32_e32 v2, v2, v3
	v_lshlrev_b32_e32 v1, 2, v1
	ds_bpermute_b32 v1, v1, v2
	v_cmp_eq_u32_e32 vcc, 0, v17
	s_and_saveexec_b64 s[0:1], vcc
	s_cbranch_execz .LBB0_25
	v_lshrrev_b32_e32 v3, 6, v0
	s_waitcnt lgkmcnt(0)
	v_max_f32_e32 v1, v1, v1
	v_max_f32_e32 v2, v2, v2
	v_lshlrev_b32_e32 v3, 2, v3
	v_max_f32_e32 v1, v2, v1
	ds_write_b32 v3, v1 offset:51200
.LBB0_25:
	s_or_b64 exec, exec, s[0:1]
	v_cmp_eq_u32_e32 vcc, 0, v0
	s_waitcnt lgkmcnt(0)
	s_barrier
	s_and_saveexec_b64 s[0:1], vcc
	s_cbranch_execz .LBB0_27
	v_mov_b32_e32 v4, 0
	ds_read_b128 v[0:3], v4 offset:51200
	ds_read_b128 v[4:7], v4 offset:51216
	s_lshl_b32 s0, s20, 2
	s_lshl_b32 s1, s6, 5
	s_or_b32 s0, s1, s0
	s_waitcnt lgkmcnt(1)
	v_max_f32_e32 v1, v1, v1
	v_max_f32_e32 v0, v0, v0
	v_max_f32_e32 v0, v0, v1
	v_max3_f32 v0, v0, v2, v3
	s_waitcnt lgkmcnt(0)
	v_max3_f32 v0, v0, v4, v5
	v_max3_f32 v0, v0, v6, v7
	v_mov_b32_e32 v1, s0
	global_store_dword v1, v0, s[4:5]

	.amdhsa_kernel _Z11proj_kernelPKfS0_S0_S0_S0_S0_S0_S0_S0_S0_S0_S0_S0_PfS1_PDF16_S1_S0_S0_S2_
		.amdhsa_group_segment_fixed_size 51232
		.amdhsa_private_segment_fixed_size 0
		.amdhsa_kernarg_size 160
		.amdhsa_user_sgpr_count 2
		.amdhsa_user_sgpr_dispatch_ptr 0
		.amdhsa_user_sgpr_queue_ptr 0
		.amdhsa_user_sgpr_kernarg_segment_ptr 1
		.amdhsa_user_sgpr_dispatch_id 0
		.amdhsa_user_sgpr_kernarg_preload_length 0
		.amdhsa_user_sgpr_kernarg_preload_offset 0
		.amdhsa_user_sgpr_private_segment_size 0
		.amdhsa_uses_dynamic_stack 0
		.amdhsa_enable_private_segment 0
		.amdhsa_system_sgpr_workgroup_id_x 1
		.amdhsa_system_sgpr_workgroup_id_y 0
		.amdhsa_system_sgpr_workgroup_id_z 0
		.amdhsa_system_sgpr_workgroup_info 0
		.amdhsa_system_vgpr_workitem_id 0
		.amdhsa_next_free_vgpr 133
		.amdhsa_next_free_sgpr 91
		.amdhsa_accum_offset 136
		.amdhsa_reserve_vcc 1
		.amdhsa_float_round_mode_32 0
		.amdhsa_float_round_mode_16_64 0
		.amdhsa_float_denorm_mode_32 3
		.amdhsa_float_denorm_mode_16_64 3
		.amdhsa_dx10_clamp 1
		.amdhsa_ieee_mode 1
		.amdhsa_fp16_overflow 0
		.amdhsa_tg_split 0
		.amdhsa_exception_fp_ieee_invalid_op 0
		.amdhsa_exception_fp_denorm_src 0
		.amdhsa_exception_fp_ieee_div_zero 0
		.amdhsa_exception_fp_ieee_overflow 0
		.amdhsa_exception_fp_ieee_underflow 0
		.amdhsa_exception_fp_ieee_inexact 0
		.amdhsa_exception_int_div_zero 0
	.end_amdhsa_kernel

amdhsa.kernels:
  - .agpr_count:     0
    .args:
      - .actual_access:  read_only
        .address_space:  global
        .offset:         0
        .size:           8
        .value_kind:     global_buffer
      - .actual_access:  read_only
        .address_space:  global
        .offset:         8
        .size:           8
        .value_kind:     global_buffer
      - .actual_access:  read_only
        .address_space:  global
        .offset:         16
        .size:           8
        .value_kind:     global_buffer
      - .actual_access:  read_only
        .address_space:  global
        .offset:         24
        .size:           8
        .value_kind:     global_buffer
      - .address_space:  global
        .offset:         32
        .size:           8
        .value_kind:     global_buffer
      - .actual_access:  read_only
        .address_space:  global
        .offset:         40
        .size:           8
        .value_kind:     global_buffer
      - .address_space:  global
        .offset:         48
        .size:           8
        .value_kind:     global_buffer
      - .actual_access:  read_only
        .address_space:  global
        .offset:         56
        .size:           8
        .value_kind:     global_buffer
      - .address_space:  global
        .offset:         64
        .size:           8
        .value_kind:     global_buffer
      - .address_space:  global
        .offset:         72
        .size:           8
        .value_kind:     global_buffer
      - .address_space:  global
        .offset:         80
        .size:           8
        .value_kind:     global_buffer
      - .address_space:  global
        .offset:         88
        .size:           8
        .value_kind:     global_buffer
      - .address_space:  global
        .offset:         96
        .size:           8
        .value_kind:     global_buffer
      - .actual_access:  write_only
        .address_space:  global
        .offset:         104
        .size:           8
        .value_kind:     global_buffer
      - .actual_access:  write_only
        .address_space:  global
        .offset:         112
        .size:           8
        .value_kind:     global_buffer
      - .actual_access:  write_only
        .address_space:  global
        .offset:         120
        .size:           8
        .value_kind:     global_buffer
      - .actual_access:  write_only
        .address_space:  global
        .offset:         128
        .size:           8
        .value_kind:     global_buffer
      - .address_space:  global
        .offset:         136
        .size:           8
        .value_kind:     global_buffer
      - .address_space:  global
        .offset:         144
        .size:           8
        .value_kind:     global_buffer
      - .actual_access:  write_only
        .address_space:  global
        .offset:         152
        .size:           8
        .value_kind:     global_buffer
    .group_segment_fixed_size: 51232
    .kernarg_segment_align: 8
    .kernarg_segment_size: 160
    .language:       OpenCL C
    .language_version:
      - 2
      - 0
    .max_flat_workgroup_size: 512
    .name:           _Z11proj_kernelPKfS0_S0_S0_S0_S0_S0_S0_S0_S0_S0_S0_S0_PfS1_PDF16_S1_S0_S0_S2_
    .private_segment_fixed_size: 0
    .sgpr_count:     33
    .sgpr_spill_count: 0
    .symbol:         _Z11proj_kernelPKfS0_S0_S0_S0_S0_S0_S0_S0_S0_S0_S0_S0_PfS1_PDF16_S1_S0_S0_S2_.kd
    .uniform_work_group_size: 1
    .uses_dynamic_stack: false
    .vgpr_count:     133
    .vgpr_spill_count: 0
    .wavefront_size: 64
  - .agpr_count:     0
    .args:
      - .actual_access:  read_only
        .address_space:  global
        .offset:         0
        .size:           8
        .value_kind:     global_buffer
      - .actual_access:  read_only
        .address_space:  global
        .offset:         8
        .size:           8
        .value_kind:     global_buffer
      - .actual_access:  read_only
        .address_space:  global
        .offset:         16
        .size:           8
        .value_kind:     global_buffer
      - .actual_access:  read_only
        .address_space:  global
        .offset:         24
        .size:           8
        .value_kind:     global_buffer
      - .actual_access:  read_only
        .address_space:  global
        .offset:         32
        .size:           8
        .value_kind:     global_buffer
      - .actual_access:  read_only
        .address_space:  global
        .offset:         40
        .size:           8
        .value_kind:     global_buffer
      - .actual_access:  read_only
        .address_space:  global
        .offset:         48
        .size:           8
        .value_kind:     global_buffer
      - .actual_access:  write_only
        .address_space:  global
        .offset:         56
        .size:           8
        .value_kind:     global_buffer
      - .actual_access:  write_only
        .address_space:  global
        .offset:         64
        .size:           8
        .value_kind:     global_buffer
    .group_segment_fixed_size: 0
    .kernarg_segment_align: 8
    .kernarg_segment_size: 72
    .language:       OpenCL C
    .language_version:
      - 2
      - 0
    .max_flat_workgroup_size: 768
    .name:           _Z11attn_kernelPKfS0_PKDF16_S0_S0_S0_S2_PDF16_S3_
    .private_segment_fixed_size: 0
    .sgpr_count:     70
    .sgpr_spill_count: 0
    .symbol:         _Z11attn_kernelPKfS0_PKDF16_S0_S0_S0_S2_PDF16_S3_.kd
    .uniform_work_group_size: 1
    .uses_dynamic_stack: false
    .vgpr_count:     168
    .vgpr_spill_count: 0
    .wavefront_size: 64
  - .agpr_count:     8
    .args:
      - .actual_access:  read_only
        .address_space:  global
        .offset:         0
        .size:           8
        .value_kind:     global_buffer
      - .actual_access:  read_only
        .address_space:  global
        .offset:         8
        .size:           8
        .value_kind:     global_buffer
      - .actual_access:  read_only
        .address_space:  global
        .offset:         16
        .size:           8
        .value_kind:     global_buffer
      - .actual_access:  write_only
        .address_space:  global
        .offset:         24
        .size:           8
        .value_kind:     global_buffer
    .group_segment_fixed_size: 27648
    .kernarg_segment_align: 8
    .kernarg_segment_size: 32
    .language:       OpenCL C
    .language_version:
      - 2
      - 0
    .max_flat_workgroup_size: 256
    .name:           _Z10out_kernelPKDF16_S0_PKfPf
    .private_segment_fixed_size: 0
    .sgpr_count:     18
    .sgpr_spill_count: 0
    .symbol:         _Z10out_kernelPKDF16_S0_PKfPf.kd
    .uniform_work_group_size: 1
    .uses_dynamic_stack: false
    .vgpr_count:     96
    .vgpr_spill_count: 0
    .wavefront_size: 64
